# attention loop on 5-slot K/V LDS rings unrolled x10 with one workgroup barrier every two key tiles; LDS writes and tile loads spread over MFMA gaps
# speedup vs baseline: 1.0648x; 1.0037x over previous
.LBB0_1138:
	v_mov_b32_e32 v224, 0
	s_mov_b32 s1, 0
	v_mov_b32_e32 v36, 0
	v_mov_b32_e32 v37, 0
	v_mov_b32_e32 v38, 0
	v_mov_b32_e32 v39, 0
	v_mov_b32_e32 v40, 0
	v_mov_b32_e32 v41, 0
	v_mov_b32_e32 v42, 0
	v_mov_b32_e32 v43, 0
	v_mov_b32_e32 v44, 0
	v_mov_b32_e32 v45, 0
	v_mov_b32_e32 v46, 0
	v_mov_b32_e32 v47, 0
	v_mov_b32_e32 v48, 0
	v_mov_b32_e32 v49, 0
	v_mov_b32_e32 v50, 0
	v_mov_b32_e32 v51, 0
	v_mov_b32_e32 v52, 0
	v_mov_b32_e32 v53, 0
	v_mov_b32_e32 v54, 0
	v_mov_b32_e32 v55, 0
	v_mov_b32_e32 v56, 0
	v_mov_b32_e32 v57, 0
	v_mov_b32_e32 v58, 0
	v_mov_b32_e32 v59, 0
	v_mov_b32_e32 v60, 0
	v_mov_b32_e32 v61, 0
	v_mov_b32_e32 v62, 0
	v_mov_b32_e32 v63, 0
	v_mov_b32_e32 v64, 0
	v_mov_b32_e32 v65, 0
	v_mov_b32_e32 v66, 0
	v_mov_b32_e32 v67, 0
	v_add_u32_e32 v178, v218, v217
	v_add_u32_e32 v230, 0x10000, v205
	v_add_u32_e32 v231, 0x10000, v178
	v_add_u32_e32 v232, 0x10000, v219
	v_add_u32_e32 v233, 0x10000, v220
	v_add_u32_e32 v234, 0x10000, v221
	v_add_u32_e32 v235, 0x10000, v222
	ds_read_b128 v[166:169], v205 offset:13312
	ds_read_b128 v[170:173], v205 offset:19968
	ds_read_b128 v[174:177], v205 offset:13344
	ds_read_b128 v[206:209], v205 offset:20000
	ds_read_b128 v[226:229], v205 offset:13376
	s_add_i32 s2, s23, s1
	s_add_i32 s3, s2, 2
	s_add_i32 s2, s2, 1
	s_cmp_ge_u32 s2, s34
	s_cselect_b32 s7, s34, 0
	s_sub_i32 s2, s2, s7
	s_cmp_ge_u32 s3, s34
	s_cselect_b32 s7, s34, 0
	s_sub_i32 s3, s3, s7
	s_cmp_ge_u32 s3, s34
	s_cselect_b32 s7, s34, 0
	s_sub_i32 s3, s3, s7
	v_lshl_add_u32 v116, s3, v215, v223
	global_load_dwordx4 v[116:119], v116, s[44:45]
	v_mad_u32_u24 v120, s3, v199, v202
	global_load_dwordx2 v[120:121], v120, s[44:45]
	s_add_i32 s2, s23, s1
	s_add_i32 s3, s2, 3
	s_add_i32 s2, s2, 1
	s_cmp_ge_u32 s2, s34
	s_cselect_b32 s7, s34, 0
	s_sub_i32 s2, s2, s7
	s_cmp_ge_u32 s3, s34
	s_cselect_b32 s7, s34, 0
	s_sub_i32 s3, s3, s7
	s_cmp_ge_u32 s3, s34
	s_cselect_b32 s7, s34, 0
	s_sub_i32 s3, s3, s7
	v_lshl_add_u32 v122, s3, v215, v223
	global_load_dwordx4 v[122:125], v122, s[44:45]
	v_mad_u32_u24 v126, s3, v199, v202
	global_load_dwordx2 v[126:127], v126, s[44:45]
	v_lshl_add_u32 v128, s2, 7, v204
	global_load_dwordx4 v[128:131], v128, s[44:45]
	s_add_i32 s2, s23, s1
	s_add_i32 s3, s2, 4
	s_add_i32 s2, s2, 2
	s_cmp_ge_u32 s2, s34
	s_cselect_b32 s7, s34, 0
	s_sub_i32 s2, s2, s7
	s_cmp_ge_u32 s3, s34
	s_cselect_b32 s7, s34, 0
	s_sub_i32 s3, s3, s7
	s_cmp_ge_u32 s3, s34
	s_cselect_b32 s7, s34, 0
	s_sub_i32 s3, s3, s7
	v_lshl_add_u32 v156, s3, v215, v223
	global_load_dwordx4 v[156:159], v156, s[44:45]
	v_mad_u32_u24 v160, s3, v199, v202
	global_load_dwordx2 v[160:161], v160, s[44:45]
	v_lshl_add_u32 v162, s2, 7, v204
	global_load_dwordx4 v[162:165], v162, s[44:45]
	s_add_i32 s2, s23, s1
	s_add_i32 s3, s2, 5
	s_add_i32 s2, s2, 3
	s_cmp_ge_u32 s2, s34
	s_cselect_b32 s7, s34, 0
	s_sub_i32 s2, s2, s7
	s_cmp_ge_u32 s3, s34
	s_cselect_b32 s7, s34, 0
	s_sub_i32 s3, s3, s7
	s_cmp_ge_u32 s3, s34
	s_cselect_b32 s7, s34, 0
	s_sub_i32 s3, s3, s7
	s_mov_b32 s12, s3
	s_mov_b32 s13, s2
	s_waitcnt lgkmcnt(4)
	v_mfma_f32_32x32x16_bf16 v[84:99], v[166:169], v[132:135], 0
	ds_read_b128 v[166:169], v205 offset:20032
	v_exp_f32_e32 v20, v20
	v_exp_f32_e32 v4, v4
	v_exp_f32_e32 v21, v21
	v_add_f32_e32 v179, v4, v20
	v_exp_f32_e32 v5, v5
	s_waitcnt lgkmcnt(4)
	v_mfma_f32_32x32x16_bf16 v[68:83], v[170:173], v[132:135], 0
	ds_read_b128 v[170:173], v205 offset:13408
	s_waitcnt vmcnt(6)
	ds_write_b128 v219, v[116:119] offset:45056
	v_add_f32_e32 v179, v21, v179
	v_cvt_pk_bf16_f32 v100, v20, v21
	v_exp_f32_e32 v22, v22
	v_add_f32_e32 v179, v5, v179
	v_exp_f32_e32 v6, v6
	v_add_f32_e32 v179, v22, v179
	v_cvt_pk_bf16_f32 v108, v4, v5
	s_waitcnt lgkmcnt(5)
	v_mfma_f32_32x32x16_bf16 v[84:99], v[174:177], v[136:139], v[84:99]
	ds_read_b128 v[174:177], v205 offset:20064
	ds_write_b64 v220, v[120:121] offset:45056
	v_exp_f32_e32 v23, v23
	v_add_f32_e32 v179, v6, v179
	v_exp_f32_e32 v7, v7
	v_add_f32_e32 v179, v23, v179
	v_cvt_pk_bf16_f32 v101, v22, v23
	v_exp_f32_e32 v24, v24
	v_add_f32_e32 v179, v7, v179
	s_waitcnt lgkmcnt(6)
	v_mfma_f32_32x32x16_bf16 v[68:83], v[206:209], v[136:139], v[68:83]
	ds_read_b128 v[206:209], v205 offset:13440
	s_waitcnt vmcnt(4)
	ds_write_b128 v219, v[122:125] offset:58368
	v_exp_f32_e32 v8, v8
	v_add_f32_e32 v179, v24, v179
	v_cvt_pk_bf16_f32 v109, v6, v7
	v_exp_f32_e32 v25, v25
	v_add_f32_e32 v179, v8, v179
	v_exp_f32_e32 v9, v9
	s_waitcnt lgkmcnt(7)
	v_mfma_f32_32x32x16_bf16 v[84:99], v[226:229], v[140:143], v[84:99]
	ds_read_b128 v[226:229], v205 offset:20096
	ds_write_b64 v220, v[126:127] offset:58368
	v_add_f32_e32 v179, v25, v179
	v_cvt_pk_bf16_f32 v102, v24, v25
	v_exp_f32_e32 v26, v26
	v_add_f32_e32 v179, v9, v179
	v_exp_f32_e32 v10, v10
	v_add_f32_e32 v179, v26, v179
	v_cvt_pk_bf16_f32 v110, v8, v9
	s_waitcnt lgkmcnt(8)
	v_mfma_f32_32x32x16_bf16 v[68:83], v[166:169], v[140:143], v[68:83]
	ds_read_b128 v[166:169], v205 offset:13472
	s_waitcnt vmcnt(3)
	ds_write_b64 v221, v[128:129] offset:35840
	v_exp_f32_e32 v27, v27
	v_add_f32_e32 v179, v10, v179
	v_exp_f32_e32 v11, v11
	v_add_f32_e32 v179, v27, v179
	v_cvt_pk_bf16_f32 v103, v26, v27
	v_exp_f32_e32 v28, v28
	v_add_f32_e32 v179, v11, v179
	s_waitcnt lgkmcnt(9)
	v_mfma_f32_32x32x16_bf16 v[84:99], v[170:173], v[144:147], v[84:99]
	ds_read_b128 v[170:173], v205 offset:20128
	ds_write_b64 v222, v[130:131] offset:35840
	v_exp_f32_e32 v29, v29
	v_add_f32_e32 v179, v28, v179
	v_cvt_pk_bf16_f32 v111, v10, v11
	v_exp_f32_e32 v30, v30
	v_add_f32_e32 v179, v29, v179
	v_exp_f32_e32 v31, v31
	s_waitcnt lgkmcnt(9)
	v_mfma_f32_32x32x16_bf16 v[68:83], v[174:177], v[144:147], v[68:83]
	s_waitcnt vmcnt(1)
	ds_write_b128 v232, v[156:159] offset:6144
	v_add_f32_e32 v179, v30, v179
	v_cvt_pk_bf16_f32 v104, v28, v29
	v_exp_f32_e32 v32, v32
	v_add_f32_e32 v179, v31, v179
	v_exp_f32_e32 v33, v33
	v_add_f32_e32 v179, v32, v179
	v_cvt_pk_bf16_f32 v105, v30, v31
	s_waitcnt lgkmcnt(8)
	v_mfma_f32_32x32x16_bf16 v[84:99], v[206:209], v[148:151], v[84:99]
	ds_write_b64 v233, v[160:161] offset:6144
	v_exp_f32_e32 v34, v34
	v_add_f32_e32 v179, v33, v179
	v_exp_f32_e32 v35, v35
	v_add_f32_e32 v179, v34, v179
	v_cvt_pk_bf16_f32 v106, v32, v33
	v_exp_f32_e32 v12, v12
	v_add_f32_e32 v179, v35, v179
	s_waitcnt lgkmcnt(7)
	v_mfma_f32_32x32x16_bf16 v[68:83], v[226:229], v[148:151], v[68:83]
	s_waitcnt vmcnt(0)
	ds_write_b64 v234, v[162:163] offset:19456
	v_exp_f32_e32 v13, v13
	v_add_f32_e32 v179, v12, v179
	v_cvt_pk_bf16_f32 v107, v34, v35
	v_exp_f32_e32 v14, v14
	v_add_f32_e32 v179, v13, v179
	v_exp_f32_e32 v15, v15
	s_waitcnt lgkmcnt(6)
	v_mfma_f32_32x32x16_bf16 v[84:99], v[166:169], v[152:155], v[84:99]
	ds_write_b64 v235, v[164:165] offset:19456
	v_add_f32_e32 v179, v14, v179
	v_cvt_pk_bf16_f32 v112, v12, v13
	v_exp_f32_e32 v16, v16
	v_add_f32_e32 v179, v15, v179
	v_exp_f32_e32 v17, v17
	v_add_f32_e32 v179, v16, v179
	v_cvt_pk_bf16_f32 v113, v14, v15
	s_waitcnt lgkmcnt(5)
	v_mfma_f32_32x32x16_bf16 v[68:83], v[170:173], v[152:155], v[68:83]
	v_lshl_add_u32 v156, s12, v215, v223
	global_load_dwordx4 v[156:159], v156, s[44:45]
	v_mad_u32_u24 v160, s12, v199, v202
	global_load_dwordx2 v[160:161], v160, s[44:45]
	v_lshl_add_u32 v162, s13, 7, v204
	global_load_dwordx4 v[162:165], v162, s[44:45]
	s_add_i32 s12, s12, 1
	s_cmp_eq_u32 s12, s34
	s_cselect_b32 s12, 0, s12
	s_add_i32 s13, s13, 1
	s_cmp_eq_u32 s13, s34
	s_cselect_b32 s13, 0, s13
	v_exp_f32_e32 v18, v18
	v_add_f32_e32 v179, v17, v179
	v_exp_f32_e32 v19, v19
	v_add_f32_e32 v179, v18, v179
	v_cvt_pk_bf16_f32 v114, v16, v17
	v_add_f32_e32 v179, v19, v179
	v_cvt_pk_bf16_f32 v115, v18, v19
	v_add_f32_e32 v224, v224, v179
	s_add_i32 s1, s1, 1
	s_waitcnt lgkmcnt(0)
	s_barrier
	ds_read_b128 v[166:169], v205 offset:45056
	ds_read_b128 v[170:173], v205 offset:51712
	ds_read_b128 v[174:177], v205 offset:45088
	ds_read_b128 v[206:209], v205 offset:51744
	ds_read_b128 v[226:229], v205 offset:45120
	s_waitcnt lgkmcnt(0)
.Latt_u10_top:
	s_waitcnt lgkmcnt(4)
	v_mfma_f32_32x32x16_bf16 v[20:35], v[166:169], v[132:135], 0
	ds_read_b128 v[166:169], v205 offset:51776
	v_exp_f32_e32 v84, v84
	v_exp_f32_e32 v68, v68
	v_exp_f32_e32 v85, v85
	s_waitcnt lgkmcnt(4)
	v_mfma_f32_32x32x16_bf16 v[4:19], v[170:173], v[132:135], 0
	ds_read_b128 v[170:173], v205 offset:45152
	v_add_f32_e32 v179, v68, v84
	v_exp_f32_e32 v69, v69
	v_add_f32_e32 v179, v85, v179
	v_cvt_pk_bf16_f32 v116, v84, v85
	s_waitcnt lgkmcnt(4)
	v_mfma_f32_32x32x16_bf16 v[20:35], v[174:177], v[136:139], v[20:35]
	ds_read_b128 v[174:177], v205 offset:51808
	v_exp_f32_e32 v86, v86
	v_add_f32_e32 v179, v69, v179
	v_exp_f32_e32 v70, v70
	v_add_f32_e32 v179, v86, v179
	s_waitcnt lgkmcnt(4)
	v_mfma_f32_32x32x16_bf16 v[4:19], v[206:209], v[136:139], v[4:19]
	ds_read_b128 v[206:209], v205 offset:45184
	v_cvt_pk_bf16_f32 v124, v68, v69
	v_exp_f32_e32 v87, v87
	v_add_f32_e32 v179, v70, v179
	v_exp_f32_e32 v71, v71
	s_waitcnt lgkmcnt(4)
	v_mfma_f32_32x32x16_bf16 v[20:35], v[226:229], v[140:143], v[20:35]
	ds_read_b128 v[226:229], v205 offset:51840
	v_add_f32_e32 v179, v87, v179
	v_cvt_pk_bf16_f32 v117, v86, v87
	v_exp_f32_e32 v88, v88
	v_add_f32_e32 v179, v71, v179
	s_waitcnt lgkmcnt(4)
	v_mfma_f32_32x32x16_bf16 v[4:19], v[166:169], v[140:143], v[4:19]
	ds_read_b128 v[166:169], v205 offset:45216
	v_exp_f32_e32 v72, v72
	v_add_f32_e32 v179, v88, v179
	v_cvt_pk_bf16_f32 v125, v70, v71
	v_exp_f32_e32 v89, v89
	s_waitcnt lgkmcnt(4)
	v_mfma_f32_32x32x16_bf16 v[20:35], v[170:173], v[144:147], v[20:35]
	ds_read_b128 v[170:173], v205 offset:51872
	v_add_f32_e32 v179, v72, v179
	v_exp_f32_e32 v73, v73
	v_add_f32_e32 v179, v89, v179
	v_cvt_pk_bf16_f32 v118, v88, v89
	s_waitcnt lgkmcnt(4)
	v_mfma_f32_32x32x16_bf16 v[4:19], v[174:177], v[144:147], v[4:19]
	ds_read_b128 v[174:177], v178 offset:26624
	v_exp_f32_e32 v90, v90
	v_add_f32_e32 v179, v73, v179
	v_exp_f32_e32 v74, v74
	v_add_f32_e32 v179, v90, v179
	s_waitcnt lgkmcnt(4)
	v_mfma_f32_32x32x16_bf16 v[20:35], v[206:209], v[148:151], v[20:35]
	ds_read_b128 v[206:209], v178 offset:31232
	s_waitcnt vmcnt(0)
	ds_write_b128 v219, v[156:159] offset:0
	v_cvt_pk_bf16_f32 v126, v72, v73
	v_exp_f32_e32 v91, v91
	v_add_f32_e32 v179, v74, v179
	v_exp_f32_e32 v75, v75
	s_waitcnt lgkmcnt(5)
	v_mfma_f32_32x32x16_bf16 v[4:19], v[226:229], v[148:151], v[4:19]
	ds_read_b128 v[226:229], v178 offset:26656
	ds_write_b64 v220, v[160:161] offset:0
	v_add_f32_e32 v179, v91, v179
	v_cvt_pk_bf16_f32 v119, v90, v91
	v_exp_f32_e32 v92, v92
	v_add_f32_e32 v179, v75, v179
	s_waitcnt lgkmcnt(6)
	v_mfma_f32_32x32x16_bf16 v[20:35], v[166:169], v[152:155], v[20:35]
	ds_read_b128 v[166:169], v178 offset:31264
	ds_write_b64 v234, v[162:163] offset:28672
	v_exp_f32_e32 v93, v93
	v_add_f32_e32 v179, v92, v179
	v_cvt_pk_bf16_f32 v127, v74, v75
	v_exp_f32_e32 v94, v94
	s_waitcnt lgkmcnt(7)
	v_mfma_f32_32x32x16_bf16 v[4:19], v[170:173], v[152:155], v[4:19]
	ds_read_b128 v[170:173], v178 offset:26688
	ds_write_b64 v235, v[164:165] offset:28672
	v_add_f32_e32 v179, v93, v179
	v_exp_f32_e32 v95, v95
	v_add_f32_e32 v179, v94, v179
	v_cvt_pk_bf16_f32 v120, v92, v93
	s_waitcnt lgkmcnt(8)
	v_mfma_f32_32x32x16_bf16 v[36:51], v[174:177], v[100:103], v[36:51]
	ds_read_b128 v[174:177], v178 offset:31296
	v_lshl_add_u32 v156, s12, v215, v223
	global_load_dwordx4 v[156:159], v156, s[44:45]
	v_exp_f32_e32 v96, v96
	v_add_f32_e32 v179, v95, v179
	v_exp_f32_e32 v97, v97
	v_add_f32_e32 v179, v96, v179
	s_waitcnt lgkmcnt(8)
	v_mfma_f32_32x32x16_bf16 v[52:67], v[206:209], v[100:103], v[52:67]
	ds_read_b128 v[206:209], v178 offset:26720
	v_mad_u32_u24 v160, s12, v199, v202
	global_load_dwordx2 v[160:161], v160, s[44:45]
	s_add_i32 s12, s12, 1
	s_cmp_eq_u32 s12, s34
	s_cselect_b32 s12, 0, s12
	v_cvt_pk_bf16_f32 v121, v94, v95
	v_exp_f32_e32 v98, v98
	v_add_f32_e32 v179, v97, v179
	v_exp_f32_e32 v99, v99
	s_waitcnt lgkmcnt(7)
	v_mfma_f32_32x32x16_bf16 v[36:51], v[226:229], v[104:107], v[36:51]
	ds_read_b128 v[226:229], v178 offset:31328
	v_lshl_add_u32 v162, s13, 7, v204
	global_load_dwordx4 v[162:165], v162, s[44:45]
	s_add_i32 s13, s13, 1
	s_cmp_eq_u32 s13, s34
	s_cselect_b32 s13, 0, s13
	v_add_f32_e32 v179, v98, v179
	v_cvt_pk_bf16_f32 v122, v96, v97
	v_exp_f32_e32 v76, v76
	v_add_f32_e32 v179, v99, v179
	s_waitcnt lgkmcnt(6)
	v_mfma_f32_32x32x16_bf16 v[52:67], v[166:169], v[104:107], v[52:67]
	ds_read_b128 v[166:169], v205 offset:58368
	v_exp_f32_e32 v77, v77
	v_add_f32_e32 v179, v76, v179
	v_cvt_pk_bf16_f32 v123, v98, v99
	v_exp_f32_e32 v78, v78
	s_waitcnt lgkmcnt(5)
	v_mfma_f32_32x32x16_bf16 v[36:51], v[170:173], v[108:111], v[36:51]
	ds_read_b128 v[170:173], v205 offset:65024
	v_add_f32_e32 v179, v77, v179
	v_exp_f32_e32 v79, v79
	v_add_f32_e32 v179, v78, v179
	v_cvt_pk_bf16_f32 v128, v76, v77
	s_waitcnt lgkmcnt(4)
	v_mfma_f32_32x32x16_bf16 v[52:67], v[174:177], v[108:111], v[52:67]
	ds_read_b128 v[174:177], v205 offset:58400
	v_exp_f32_e32 v80, v80
	v_add_f32_e32 v179, v79, v179
	v_exp_f32_e32 v81, v81
	v_add_f32_e32 v179, v80, v179
	s_waitcnt lgkmcnt(4)
	v_mfma_f32_32x32x16_bf16 v[36:51], v[206:209], v[112:115], v[36:51]
	ds_read_b128 v[206:209], v205 offset:65056
	v_cvt_pk_bf16_f32 v129, v78, v79
	v_exp_f32_e32 v82, v82
	v_add_f32_e32 v179, v81, v179
	v_exp_f32_e32 v83, v83
	s_waitcnt lgkmcnt(4)
	v_mfma_f32_32x32x16_bf16 v[52:67], v[226:229], v[112:115], v[52:67]
	ds_read_b128 v[226:229], v205 offset:58432
	v_add_f32_e32 v179, v82, v179
	v_cvt_pk_bf16_f32 v130, v80, v81
	v_add_f32_e32 v179, v83, v179
	v_cvt_pk_bf16_f32 v131, v82, v83
	v_add_f32_e32 v224, v224, v179
	s_add_i32 s1, s1, 1
	s_cmp_lt_u32 s1, s34
	s_barrier
	s_cbranch_scc0 .Latt_u10_fin1
	s_waitcnt lgkmcnt(4)
	v_mfma_f32_32x32x16_bf16 v[84:99], v[166:169], v[132:135], 0
	ds_read_b128 v[166:169], v205 offset:65088
	v_exp_f32_e32 v20, v20
	v_exp_f32_e32 v4, v4
	v_exp_f32_e32 v21, v21
	s_waitcnt lgkmcnt(4)
	v_mfma_f32_32x32x16_bf16 v[68:83], v[170:173], v[132:135], 0
	ds_read_b128 v[170:173], v205 offset:58464
	v_add_f32_e32 v179, v4, v20
	v_exp_f32_e32 v5, v5
	v_add_f32_e32 v179, v21, v179
	v_cvt_pk_bf16_f32 v100, v20, v21
	s_waitcnt lgkmcnt(4)
	v_mfma_f32_32x32x16_bf16 v[84:99], v[174:177], v[136:139], v[84:99]
	ds_read_b128 v[174:177], v205 offset:65120
	v_exp_f32_e32 v22, v22
	v_add_f32_e32 v179, v5, v179
	v_exp_f32_e32 v6, v6
	v_add_f32_e32 v179, v22, v179
	s_waitcnt lgkmcnt(4)
	v_mfma_f32_32x32x16_bf16 v[68:83], v[206:209], v[136:139], v[68:83]
	ds_read_b128 v[206:209], v205 offset:58496
	v_cvt_pk_bf16_f32 v108, v4, v5
	v_exp_f32_e32 v23, v23
	v_add_f32_e32 v179, v6, v179
	v_exp_f32_e32 v7, v7
	s_waitcnt lgkmcnt(4)
	v_mfma_f32_32x32x16_bf16 v[84:99], v[226:229], v[140:143], v[84:99]
	ds_read_b128 v[226:229], v205 offset:65152
	v_add_f32_e32 v179, v23, v179
	v_cvt_pk_bf16_f32 v101, v22, v23
	v_exp_f32_e32 v24, v24
	v_add_f32_e32 v179, v7, v179
	s_waitcnt lgkmcnt(4)
	v_mfma_f32_32x32x16_bf16 v[68:83], v[166:169], v[140:143], v[68:83]
	ds_read_b128 v[166:169], v205 offset:58528
	v_exp_f32_e32 v8, v8
	v_add_f32_e32 v179, v24, v179
	v_cvt_pk_bf16_f32 v109, v6, v7
	v_exp_f32_e32 v25, v25
	s_waitcnt lgkmcnt(4)
	v_mfma_f32_32x32x16_bf16 v[84:99], v[170:173], v[144:147], v[84:99]
	ds_read_b128 v[170:173], v205 offset:65184
	v_add_f32_e32 v179, v8, v179
	v_exp_f32_e32 v9, v9
	v_add_f32_e32 v179, v25, v179
	v_cvt_pk_bf16_f32 v102, v24, v25
	s_waitcnt lgkmcnt(4)
	v_mfma_f32_32x32x16_bf16 v[68:83], v[174:177], v[144:147], v[68:83]
	ds_read_b128 v[174:177], v178 offset:35840
	v_exp_f32_e32 v26, v26
	v_add_f32_e32 v179, v9, v179
	v_exp_f32_e32 v10, v10
	v_add_f32_e32 v179, v26, v179
	s_waitcnt lgkmcnt(4)
	v_mfma_f32_32x32x16_bf16 v[84:99], v[206:209], v[148:151], v[84:99]
	ds_read_b128 v[206:209], v178 offset:40448
	s_waitcnt vmcnt(0)
	ds_write_b128 v219, v[156:159] offset:13312
	v_cvt_pk_bf16_f32 v110, v8, v9
	v_exp_f32_e32 v27, v27
	v_add_f32_e32 v179, v10, v179
	v_exp_f32_e32 v11, v11
	s_waitcnt lgkmcnt(5)
	v_mfma_f32_32x32x16_bf16 v[68:83], v[226:229], v[148:151], v[68:83]
	ds_read_b128 v[226:229], v178 offset:35872
	ds_write_b64 v220, v[160:161] offset:13312
	v_add_f32_e32 v179, v27, v179
	v_cvt_pk_bf16_f32 v103, v26, v27
	v_exp_f32_e32 v28, v28
	v_add_f32_e32 v179, v11, v179
	s_waitcnt lgkmcnt(6)
	v_mfma_f32_32x32x16_bf16 v[84:99], v[166:169], v[152:155], v[84:99]
	ds_read_b128 v[166:169], v178 offset:40480
	ds_write_b64 v234, v[162:163] offset:37888
	v_exp_f32_e32 v29, v29
	v_add_f32_e32 v179, v28, v179
	v_cvt_pk_bf16_f32 v111, v10, v11
	v_exp_f32_e32 v30, v30
	s_waitcnt lgkmcnt(7)
	v_mfma_f32_32x32x16_bf16 v[68:83], v[170:173], v[152:155], v[68:83]
	ds_read_b128 v[170:173], v178 offset:35904
	ds_write_b64 v235, v[164:165] offset:37888
	v_add_f32_e32 v179, v29, v179
	v_exp_f32_e32 v31, v31
	v_add_f32_e32 v179, v30, v179
	v_cvt_pk_bf16_f32 v104, v28, v29
	s_waitcnt lgkmcnt(8)
	v_mfma_f32_32x32x16_bf16 v[36:51], v[174:177], v[116:119], v[36:51]
	ds_read_b128 v[174:177], v178 offset:40512
	v_lshl_add_u32 v156, s12, v215, v223
	global_load_dwordx4 v[156:159], v156, s[44:45]
	v_exp_f32_e32 v32, v32
	v_add_f32_e32 v179, v31, v179
	v_exp_f32_e32 v33, v33
	v_add_f32_e32 v179, v32, v179
	s_waitcnt lgkmcnt(8)
	v_mfma_f32_32x32x16_bf16 v[52:67], v[206:209], v[116:119], v[52:67]
	ds_read_b128 v[206:209], v178 offset:35936
	v_mad_u32_u24 v160, s12, v199, v202
	global_load_dwordx2 v[160:161], v160, s[44:45]
	s_add_i32 s12, s12, 1
	s_cmp_eq_u32 s12, s34
	s_cselect_b32 s12, 0, s12
	v_cvt_pk_bf16_f32 v105, v30, v31
	v_exp_f32_e32 v34, v34
	v_add_f32_e32 v179, v33, v179
	v_exp_f32_e32 v35, v35
	s_waitcnt lgkmcnt(7)
	v_mfma_f32_32x32x16_bf16 v[36:51], v[226:229], v[120:123], v[36:51]
	ds_read_b128 v[226:229], v178 offset:40544
	v_lshl_add_u32 v162, s13, 7, v204
	global_load_dwordx4 v[162:165], v162, s[44:45]
	s_add_i32 s13, s13, 1
	s_cmp_eq_u32 s13, s34
	s_cselect_b32 s13, 0, s13
	v_add_f32_e32 v179, v34, v179
	v_cvt_pk_bf16_f32 v106, v32, v33
	v_exp_f32_e32 v12, v12
	v_add_f32_e32 v179, v35, v179
	s_waitcnt lgkmcnt(6)
	v_mfma_f32_32x32x16_bf16 v[52:67], v[166:169], v[120:123], v[52:67]
	ds_read_b128 v[166:169], v230 offset:6144
	v_exp_f32_e32 v13, v13
	v_add_f32_e32 v179, v12, v179
	v_cvt_pk_bf16_f32 v107, v34, v35
	v_exp_f32_e32 v14, v14
	s_waitcnt lgkmcnt(5)
	v_mfma_f32_32x32x16_bf16 v[36:51], v[170:173], v[124:127], v[36:51]
	ds_read_b128 v[170:173], v230 offset:12800
	v_add_f32_e32 v179, v13, v179
	v_exp_f32_e32 v15, v15
	v_add_f32_e32 v179, v14, v179
	v_cvt_pk_bf16_f32 v112, v12, v13
	s_waitcnt lgkmcnt(4)
	v_mfma_f32_32x32x16_bf16 v[52:67], v[174:177], v[124:127], v[52:67]
	ds_read_b128 v[174:177], v230 offset:6176
	v_exp_f32_e32 v16, v16
	v_add_f32_e32 v179, v15, v179
	v_exp_f32_e32 v17, v17
	v_add_f32_e32 v179, v16, v179
	s_waitcnt lgkmcnt(4)
	v_mfma_f32_32x32x16_bf16 v[36:51], v[206:209], v[128:131], v[36:51]
	ds_read_b128 v[206:209], v230 offset:12832
	v_cvt_pk_bf16_f32 v113, v14, v15
	v_exp_f32_e32 v18, v18
	v_add_f32_e32 v179, v17, v179
	v_exp_f32_e32 v19, v19
	s_waitcnt lgkmcnt(4)
	v_mfma_f32_32x32x16_bf16 v[52:67], v[226:229], v[128:131], v[52:67]
	ds_read_b128 v[226:229], v230 offset:6208
	v_add_f32_e32 v179, v18, v179
	v_cvt_pk_bf16_f32 v114, v16, v17
	v_add_f32_e32 v179, v19, v179
	v_cvt_pk_bf16_f32 v115, v18, v19
	v_add_f32_e32 v224, v224, v179
	s_add_i32 s1, s1, 1
	s_waitcnt lgkmcnt(4)
	v_mfma_f32_32x32x16_bf16 v[20:35], v[166:169], v[132:135], 0
	ds_read_b128 v[166:169], v230 offset:12864
	v_exp_f32_e32 v84, v84
	v_exp_f32_e32 v68, v68
	v_exp_f32_e32 v85, v85
	s_waitcnt lgkmcnt(4)
	v_mfma_f32_32x32x16_bf16 v[4:19], v[170:173], v[132:135], 0
	ds_read_b128 v[170:173], v230 offset:6240
	v_add_f32_e32 v179, v68, v84
	v_exp_f32_e32 v69, v69
	v_add_f32_e32 v179, v85, v179
	v_cvt_pk_bf16_f32 v116, v84, v85
	s_waitcnt lgkmcnt(4)
	v_mfma_f32_32x32x16_bf16 v[20:35], v[174:177], v[136:139], v[20:35]
	ds_read_b128 v[174:177], v230 offset:12896
	v_exp_f32_e32 v86, v86
	v_add_f32_e32 v179, v69, v179
	v_exp_f32_e32 v70, v70
	v_add_f32_e32 v179, v86, v179
	s_waitcnt lgkmcnt(4)
	v_mfma_f32_32x32x16_bf16 v[4:19], v[206:209], v[136:139], v[4:19]
	ds_read_b128 v[206:209], v230 offset:6272
	v_cvt_pk_bf16_f32 v124, v68, v69
	v_exp_f32_e32 v87, v87
	v_add_f32_e32 v179, v70, v179
	v_exp_f32_e32 v71, v71
	s_waitcnt lgkmcnt(4)
	v_mfma_f32_32x32x16_bf16 v[20:35], v[226:229], v[140:143], v[20:35]
	ds_read_b128 v[226:229], v230 offset:12928
	v_add_f32_e32 v179, v87, v179
	v_cvt_pk_bf16_f32 v117, v86, v87
	v_exp_f32_e32 v88, v88
	v_add_f32_e32 v179, v71, v179
	s_waitcnt lgkmcnt(4)
	v_mfma_f32_32x32x16_bf16 v[4:19], v[166:169], v[140:143], v[4:19]
	ds_read_b128 v[166:169], v230 offset:6304
	v_exp_f32_e32 v72, v72
	v_add_f32_e32 v179, v88, v179
	v_cvt_pk_bf16_f32 v125, v70, v71
	v_exp_f32_e32 v89, v89
	s_waitcnt lgkmcnt(4)
	v_mfma_f32_32x32x16_bf16 v[20:35], v[170:173], v[144:147], v[20:35]
	ds_read_b128 v[170:173], v230 offset:12960
	v_add_f32_e32 v179, v72, v179
	v_exp_f32_e32 v73, v73
	v_add_f32_e32 v179, v89, v179
	v_cvt_pk_bf16_f32 v118, v88, v89
	s_waitcnt lgkmcnt(4)
	v_mfma_f32_32x32x16_bf16 v[4:19], v[174:177], v[144:147], v[4:19]
	ds_read_b128 v[174:177], v231 offset:19456
	v_exp_f32_e32 v90, v90
	v_add_f32_e32 v179, v73, v179
	v_exp_f32_e32 v74, v74
	v_add_f32_e32 v179, v90, v179
	s_waitcnt lgkmcnt(4)
	v_mfma_f32_32x32x16_bf16 v[20:35], v[206:209], v[148:151], v[20:35]
	ds_read_b128 v[206:209], v231 offset:24064
	s_waitcnt vmcnt(0)
	ds_write_b128 v219, v[156:159] offset:45056
	v_cvt_pk_bf16_f32 v126, v72, v73
	v_exp_f32_e32 v91, v91
	v_add_f32_e32 v179, v74, v179
	v_exp_f32_e32 v75, v75
	s_waitcnt lgkmcnt(5)
	v_mfma_f32_32x32x16_bf16 v[4:19], v[226:229], v[148:151], v[4:19]
	ds_read_b128 v[226:229], v231 offset:19488
	ds_write_b64 v220, v[160:161] offset:45056
	v_add_f32_e32 v179, v91, v179
	v_cvt_pk_bf16_f32 v119, v90, v91
	v_exp_f32_e32 v92, v92
	v_add_f32_e32 v179, v75, v179
	s_waitcnt lgkmcnt(6)
	v_mfma_f32_32x32x16_bf16 v[20:35], v[166:169], v[152:155], v[20:35]
	ds_read_b128 v[166:169], v231 offset:24096
	ds_write_b64 v221, v[162:163] offset:26624
	v_exp_f32_e32 v93, v93
	v_add_f32_e32 v179, v92, v179
	v_cvt_pk_bf16_f32 v127, v74, v75
	v_exp_f32_e32 v94, v94
	s_waitcnt lgkmcnt(7)
	v_mfma_f32_32x32x16_bf16 v[4:19], v[170:173], v[152:155], v[4:19]
	ds_read_b128 v[170:173], v231 offset:19520
	ds_write_b64 v222, v[164:165] offset:26624
	v_add_f32_e32 v179, v93, v179
	v_exp_f32_e32 v95, v95
	v_add_f32_e32 v179, v94, v179
	v_cvt_pk_bf16_f32 v120, v92, v93
	s_waitcnt lgkmcnt(8)
	v_mfma_f32_32x32x16_bf16 v[36:51], v[174:177], v[100:103], v[36:51]
	ds_read_b128 v[174:177], v231 offset:24128
	v_lshl_add_u32 v156, s12, v215, v223
	global_load_dwordx4 v[156:159], v156, s[44:45]
	v_exp_f32_e32 v96, v96
	v_add_f32_e32 v179, v95, v179
	v_exp_f32_e32 v97, v97
	v_add_f32_e32 v179, v96, v179
	s_waitcnt lgkmcnt(8)
	v_mfma_f32_32x32x16_bf16 v[52:67], v[206:209], v[100:103], v[52:67]
	ds_read_b128 v[206:209], v231 offset:19552
	v_mad_u32_u24 v160, s12, v199, v202
	global_load_dwordx2 v[160:161], v160, s[44:45]
	s_add_i32 s12, s12, 1
	s_cmp_eq_u32 s12, s34
	s_cselect_b32 s12, 0, s12
	v_cvt_pk_bf16_f32 v121, v94, v95
	v_exp_f32_e32 v98, v98
	v_add_f32_e32 v179, v97, v179
	v_exp_f32_e32 v99, v99
	s_waitcnt lgkmcnt(7)
	v_mfma_f32_32x32x16_bf16 v[36:51], v[226:229], v[104:107], v[36:51]
	ds_read_b128 v[226:229], v231 offset:24160
	v_lshl_add_u32 v162, s13, 7, v204
	global_load_dwordx4 v[162:165], v162, s[44:45]
	s_add_i32 s13, s13, 1
	s_cmp_eq_u32 s13, s34
	s_cselect_b32 s13, 0, s13
	v_add_f32_e32 v179, v98, v179
	v_cvt_pk_bf16_f32 v122, v96, v97
	v_exp_f32_e32 v76, v76
	v_add_f32_e32 v179, v99, v179
	s_waitcnt lgkmcnt(6)
	v_mfma_f32_32x32x16_bf16 v[52:67], v[166:169], v[104:107], v[52:67]
	ds_read_b128 v[166:169], v205
	v_exp_f32_e32 v77, v77
	v_add_f32_e32 v179, v76, v179
	v_cvt_pk_bf16_f32 v123, v98, v99
	v_exp_f32_e32 v78, v78
	s_waitcnt lgkmcnt(5)
	v_mfma_f32_32x32x16_bf16 v[36:51], v[170:173], v[108:111], v[36:51]
	ds_read_b128 v[170:173], v205 offset:6656
	v_add_f32_e32 v179, v77, v179
	v_exp_f32_e32 v79, v79
	v_add_f32_e32 v179, v78, v179
	v_cvt_pk_bf16_f32 v128, v76, v77
	s_waitcnt lgkmcnt(4)
	v_mfma_f32_32x32x16_bf16 v[52:67], v[174:177], v[108:111], v[52:67]
	ds_read_b128 v[174:177], v205 offset:32
	v_exp_f32_e32 v80, v80
	v_add_f32_e32 v179, v79, v179
	v_exp_f32_e32 v81, v81
	v_add_f32_e32 v179, v80, v179
	s_waitcnt lgkmcnt(4)
	v_mfma_f32_32x32x16_bf16 v[36:51], v[206:209], v[112:115], v[36:51]
	ds_read_b128 v[206:209], v205 offset:6688
	v_cvt_pk_bf16_f32 v129, v78, v79
	v_exp_f32_e32 v82, v82
	v_add_f32_e32 v179, v81, v179
	v_exp_f32_e32 v83, v83
	s_waitcnt lgkmcnt(4)
	v_mfma_f32_32x32x16_bf16 v[52:67], v[226:229], v[112:115], v[52:67]
	ds_read_b128 v[226:229], v205 offset:64
	v_add_f32_e32 v179, v82, v179
	v_cvt_pk_bf16_f32 v130, v80, v81
	v_add_f32_e32 v179, v83, v179
	v_cvt_pk_bf16_f32 v131, v82, v83
	v_add_f32_e32 v224, v224, v179
	s_add_i32 s1, s1, 1
	s_cmp_lt_u32 s1, s34
	s_barrier
	s_cbranch_scc0 .Latt_u10_fin3
	s_waitcnt lgkmcnt(4)
	v_mfma_f32_32x32x16_bf16 v[84:99], v[166:169], v[132:135], 0
	ds_read_b128 v[166:169], v205 offset:6720
	v_exp_f32_e32 v20, v20
	v_exp_f32_e32 v4, v4
	v_exp_f32_e32 v21, v21
	s_waitcnt lgkmcnt(4)
	v_mfma_f32_32x32x16_bf16 v[68:83], v[170:173], v[132:135], 0
	ds_read_b128 v[170:173], v205 offset:96
	v_add_f32_e32 v179, v4, v20
	v_exp_f32_e32 v5, v5
	v_add_f32_e32 v179, v21, v179
	v_cvt_pk_bf16_f32 v100, v20, v21
	s_waitcnt lgkmcnt(4)
	v_mfma_f32_32x32x16_bf16 v[84:99], v[174:177], v[136:139], v[84:99]
	ds_read_b128 v[174:177], v205 offset:6752
	v_exp_f32_e32 v22, v22
	v_add_f32_e32 v179, v5, v179
	v_exp_f32_e32 v6, v6
	v_add_f32_e32 v179, v22, v179
	s_waitcnt lgkmcnt(4)
	v_mfma_f32_32x32x16_bf16 v[68:83], v[206:209], v[136:139], v[68:83]
	ds_read_b128 v[206:209], v205 offset:128
	v_cvt_pk_bf16_f32 v108, v4, v5
	v_exp_f32_e32 v23, v23
	v_add_f32_e32 v179, v6, v179
	v_exp_f32_e32 v7, v7
	s_waitcnt lgkmcnt(4)
	v_mfma_f32_32x32x16_bf16 v[84:99], v[226:229], v[140:143], v[84:99]
	ds_read_b128 v[226:229], v205 offset:6784
	v_add_f32_e32 v179, v23, v179
	v_cvt_pk_bf16_f32 v101, v22, v23
	v_exp_f32_e32 v24, v24
	v_add_f32_e32 v179, v7, v179
	s_waitcnt lgkmcnt(4)
	v_mfma_f32_32x32x16_bf16 v[68:83], v[166:169], v[140:143], v[68:83]
	ds_read_b128 v[166:169], v205 offset:160
	v_exp_f32_e32 v8, v8
	v_add_f32_e32 v179, v24, v179
	v_cvt_pk_bf16_f32 v109, v6, v7
	v_exp_f32_e32 v25, v25
	s_waitcnt lgkmcnt(4)
	v_mfma_f32_32x32x16_bf16 v[84:99], v[170:173], v[144:147], v[84:99]
	ds_read_b128 v[170:173], v205 offset:6816
	v_add_f32_e32 v179, v8, v179
	v_exp_f32_e32 v9, v9
	v_add_f32_e32 v179, v25, v179
	v_cvt_pk_bf16_f32 v102, v24, v25
	s_waitcnt lgkmcnt(4)
	v_mfma_f32_32x32x16_bf16 v[68:83], v[174:177], v[144:147], v[68:83]
	ds_read_b128 v[174:177], v231 offset:28672
	v_exp_f32_e32 v26, v26
	v_add_f32_e32 v179, v9, v179
	v_exp_f32_e32 v10, v10
	v_add_f32_e32 v179, v26, v179
	s_waitcnt lgkmcnt(4)
	v_mfma_f32_32x32x16_bf16 v[84:99], v[206:209], v[148:151], v[84:99]
	ds_read_b128 v[206:209], v231 offset:33280
	s_waitcnt vmcnt(0)
	ds_write_b128 v219, v[156:159] offset:58368
	v_cvt_pk_bf16_f32 v110, v8, v9
	v_exp_f32_e32 v27, v27
	v_add_f32_e32 v179, v10, v179
	v_exp_f32_e32 v11, v11
	s_waitcnt lgkmcnt(5)
	v_mfma_f32_32x32x16_bf16 v[68:83], v[226:229], v[148:151], v[68:83]
	ds_read_b128 v[226:229], v231 offset:28704
	ds_write_b64 v220, v[160:161] offset:58368
	v_add_f32_e32 v179, v27, v179
	v_cvt_pk_bf16_f32 v103, v26, v27
	v_exp_f32_e32 v28, v28
	v_add_f32_e32 v179, v11, v179
	s_waitcnt lgkmcnt(6)
	v_mfma_f32_32x32x16_bf16 v[84:99], v[166:169], v[152:155], v[84:99]
	ds_read_b128 v[166:169], v231 offset:33312
	ds_write_b64 v221, v[162:163] offset:35840
	v_exp_f32_e32 v29, v29
	v_add_f32_e32 v179, v28, v179
	v_cvt_pk_bf16_f32 v111, v10, v11
	v_exp_f32_e32 v30, v30
	s_waitcnt lgkmcnt(7)
	v_mfma_f32_32x32x16_bf16 v[68:83], v[170:173], v[152:155], v[68:83]
	ds_read_b128 v[170:173], v231 offset:28736
	ds_write_b64 v222, v[164:165] offset:35840
	v_add_f32_e32 v179, v29, v179
	v_exp_f32_e32 v31, v31
	v_add_f32_e32 v179, v30, v179
	v_cvt_pk_bf16_f32 v104, v28, v29
	s_waitcnt lgkmcnt(8)
	v_mfma_f32_32x32x16_bf16 v[36:51], v[174:177], v[116:119], v[36:51]
	ds_read_b128 v[174:177], v231 offset:33344
	v_lshl_add_u32 v156, s12, v215, v223
	global_load_dwordx4 v[156:159], v156, s[44:45]
	v_exp_f32_e32 v32, v32
	v_add_f32_e32 v179, v31, v179
	v_exp_f32_e32 v33, v33
	v_add_f32_e32 v179, v32, v179
	s_waitcnt lgkmcnt(8)
	v_mfma_f32_32x32x16_bf16 v[52:67], v[206:209], v[116:119], v[52:67]
	ds_read_b128 v[206:209], v231 offset:28768
	v_mad_u32_u24 v160, s12, v199, v202
	global_load_dwordx2 v[160:161], v160, s[44:45]
	s_add_i32 s12, s12, 1
	s_cmp_eq_u32 s12, s34
	s_cselect_b32 s12, 0, s12
	v_cvt_pk_bf16_f32 v105, v30, v31
	v_exp_f32_e32 v34, v34
	v_add_f32_e32 v179, v33, v179
	v_exp_f32_e32 v35, v35
	s_waitcnt lgkmcnt(7)
	v_mfma_f32_32x32x16_bf16 v[36:51], v[226:229], v[120:123], v[36:51]
	ds_read_b128 v[226:229], v231 offset:33376
	v_lshl_add_u32 v162, s13, 7, v204
	global_load_dwordx4 v[162:165], v162, s[44:45]
	s_add_i32 s13, s13, 1
	s_cmp_eq_u32 s13, s34
	s_cselect_b32 s13, 0, s13
	v_add_f32_e32 v179, v34, v179
	v_cvt_pk_bf16_f32 v106, v32, v33
	v_exp_f32_e32 v12, v12
	v_add_f32_e32 v179, v35, v179
	s_waitcnt lgkmcnt(6)
	v_mfma_f32_32x32x16_bf16 v[52:67], v[166:169], v[120:123], v[52:67]
	ds_read_b128 v[166:169], v205 offset:13312
	v_exp_f32_e32 v13, v13
	v_add_f32_e32 v179, v12, v179
	v_cvt_pk_bf16_f32 v107, v34, v35
	v_exp_f32_e32 v14, v14
	s_waitcnt lgkmcnt(5)
	v_mfma_f32_32x32x16_bf16 v[36:51], v[170:173], v[124:127], v[36:51]
	ds_read_b128 v[170:173], v205 offset:19968
	v_add_f32_e32 v179, v13, v179
	v_exp_f32_e32 v15, v15
	v_add_f32_e32 v179, v14, v179
	v_cvt_pk_bf16_f32 v112, v12, v13
	s_waitcnt lgkmcnt(4)
	v_mfma_f32_32x32x16_bf16 v[52:67], v[174:177], v[124:127], v[52:67]
	ds_read_b128 v[174:177], v205 offset:13344
	v_exp_f32_e32 v16, v16
	v_add_f32_e32 v179, v15, v179
	v_exp_f32_e32 v17, v17
	v_add_f32_e32 v179, v16, v179
	s_waitcnt lgkmcnt(4)
	v_mfma_f32_32x32x16_bf16 v[36:51], v[206:209], v[128:131], v[36:51]
	ds_read_b128 v[206:209], v205 offset:20000
	v_cvt_pk_bf16_f32 v113, v14, v15
	v_exp_f32_e32 v18, v18
	v_add_f32_e32 v179, v17, v179
	v_exp_f32_e32 v19, v19
	s_waitcnt lgkmcnt(4)
	v_mfma_f32_32x32x16_bf16 v[52:67], v[226:229], v[128:131], v[52:67]
	ds_read_b128 v[226:229], v205 offset:13376
	v_add_f32_e32 v179, v18, v179
	v_cvt_pk_bf16_f32 v114, v16, v17
	v_add_f32_e32 v179, v19, v179
	v_cvt_pk_bf16_f32 v115, v18, v19
	v_add_f32_e32 v224, v224, v179
	s_add_i32 s1, s1, 1
	s_waitcnt lgkmcnt(4)
	v_mfma_f32_32x32x16_bf16 v[20:35], v[166:169], v[132:135], 0
	ds_read_b128 v[166:169], v205 offset:20032
	v_exp_f32_e32 v84, v84
	v_exp_f32_e32 v68, v68
	v_exp_f32_e32 v85, v85
	s_waitcnt lgkmcnt(4)
	v_mfma_f32_32x32x16_bf16 v[4:19], v[170:173], v[132:135], 0
	ds_read_b128 v[170:173], v205 offset:13408
	v_add_f32_e32 v179, v68, v84
	v_exp_f32_e32 v69, v69
	v_add_f32_e32 v179, v85, v179
	v_cvt_pk_bf16_f32 v116, v84, v85
	s_waitcnt lgkmcnt(4)
	v_mfma_f32_32x32x16_bf16 v[20:35], v[174:177], v[136:139], v[20:35]
	ds_read_b128 v[174:177], v205 offset:20064
	v_exp_f32_e32 v86, v86
	v_add_f32_e32 v179, v69, v179
	v_exp_f32_e32 v70, v70
	v_add_f32_e32 v179, v86, v179
	s_waitcnt lgkmcnt(4)
	v_mfma_f32_32x32x16_bf16 v[4:19], v[206:209], v[136:139], v[4:19]
	ds_read_b128 v[206:209], v205 offset:13440
	v_cvt_pk_bf16_f32 v124, v68, v69
	v_exp_f32_e32 v87, v87
	v_add_f32_e32 v179, v70, v179
	v_exp_f32_e32 v71, v71
	s_waitcnt lgkmcnt(4)
	v_mfma_f32_32x32x16_bf16 v[20:35], v[226:229], v[140:143], v[20:35]
	ds_read_b128 v[226:229], v205 offset:20096
	v_add_f32_e32 v179, v87, v179
	v_cvt_pk_bf16_f32 v117, v86, v87
	v_exp_f32_e32 v88, v88
	v_add_f32_e32 v179, v71, v179
	s_waitcnt lgkmcnt(4)
	v_mfma_f32_32x32x16_bf16 v[4:19], v[166:169], v[140:143], v[4:19]
	ds_read_b128 v[166:169], v205 offset:13472
	v_exp_f32_e32 v72, v72
	v_add_f32_e32 v179, v88, v179
	v_cvt_pk_bf16_f32 v125, v70, v71
	v_exp_f32_e32 v89, v89
	s_waitcnt lgkmcnt(4)
	v_mfma_f32_32x32x16_bf16 v[20:35], v[170:173], v[144:147], v[20:35]
	ds_read_b128 v[170:173], v205 offset:20128
	v_add_f32_e32 v179, v72, v179
	v_exp_f32_e32 v73, v73
	v_add_f32_e32 v179, v89, v179
	v_cvt_pk_bf16_f32 v118, v88, v89
	s_waitcnt lgkmcnt(4)
	v_mfma_f32_32x32x16_bf16 v[4:19], v[174:177], v[144:147], v[4:19]
	ds_read_b128 v[174:177], v231 offset:37888
	v_exp_f32_e32 v90, v90
	v_add_f32_e32 v179, v73, v179
	v_exp_f32_e32 v74, v74
	v_add_f32_e32 v179, v90, v179
	s_waitcnt lgkmcnt(4)
	v_mfma_f32_32x32x16_bf16 v[20:35], v[206:209], v[148:151], v[20:35]
	ds_read_b128 v[206:209], v231 offset:42496
	s_waitcnt vmcnt(0)
	ds_write_b128 v232, v[156:159] offset:6144
	v_cvt_pk_bf16_f32 v126, v72, v73
	v_exp_f32_e32 v91, v91
	v_add_f32_e32 v179, v74, v179
	v_exp_f32_e32 v75, v75
	s_waitcnt lgkmcnt(5)
	v_mfma_f32_32x32x16_bf16 v[4:19], v[226:229], v[148:151], v[4:19]
	ds_read_b128 v[226:229], v231 offset:37920
	ds_write_b64 v233, v[160:161] offset:6144
	v_add_f32_e32 v179, v91, v179
	v_cvt_pk_bf16_f32 v119, v90, v91
	v_exp_f32_e32 v92, v92
	v_add_f32_e32 v179, v75, v179
	s_waitcnt lgkmcnt(6)
	v_mfma_f32_32x32x16_bf16 v[20:35], v[166:169], v[152:155], v[20:35]
	ds_read_b128 v[166:169], v231 offset:42528
	ds_write_b64 v234, v[162:163] offset:19456
	v_exp_f32_e32 v93, v93
	v_add_f32_e32 v179, v92, v179
	v_cvt_pk_bf16_f32 v127, v74, v75
	v_exp_f32_e32 v94, v94
	s_waitcnt lgkmcnt(7)
	v_mfma_f32_32x32x16_bf16 v[4:19], v[170:173], v[152:155], v[4:19]
	ds_read_b128 v[170:173], v231 offset:37952
	ds_write_b64 v235, v[164:165] offset:19456
	v_add_f32_e32 v179, v93, v179
	v_exp_f32_e32 v95, v95
	v_add_f32_e32 v179, v94, v179
	v_cvt_pk_bf16_f32 v120, v92, v93
	s_waitcnt lgkmcnt(8)
	v_mfma_f32_32x32x16_bf16 v[36:51], v[174:177], v[100:103], v[36:51]
	ds_read_b128 v[174:177], v231 offset:42560
	v_lshl_add_u32 v156, s12, v215, v223
	global_load_dwordx4 v[156:159], v156, s[44:45]
	v_exp_f32_e32 v96, v96
	v_add_f32_e32 v179, v95, v179
	v_exp_f32_e32 v97, v97
	v_add_f32_e32 v179, v96, v179
	s_waitcnt lgkmcnt(8)
	v_mfma_f32_32x32x16_bf16 v[52:67], v[206:209], v[100:103], v[52:67]
	ds_read_b128 v[206:209], v231 offset:37984
	v_mad_u32_u24 v160, s12, v199, v202
	global_load_dwordx2 v[160:161], v160, s[44:45]
	s_add_i32 s12, s12, 1
	s_cmp_eq_u32 s12, s34
	s_cselect_b32 s12, 0, s12
	v_cvt_pk_bf16_f32 v121, v94, v95
	v_exp_f32_e32 v98, v98
	v_add_f32_e32 v179, v97, v179
	v_exp_f32_e32 v99, v99
	s_waitcnt lgkmcnt(7)
	v_mfma_f32_32x32x16_bf16 v[36:51], v[226:229], v[104:107], v[36:51]
	ds_read_b128 v[226:229], v231 offset:42592
	v_lshl_add_u32 v162, s13, 7, v204
	global_load_dwordx4 v[162:165], v162, s[44:45]
	s_add_i32 s13, s13, 1
	s_cmp_eq_u32 s13, s34
	s_cselect_b32 s13, 0, s13
	v_add_f32_e32 v179, v98, v179
	v_cvt_pk_bf16_f32 v122, v96, v97
	v_exp_f32_e32 v76, v76
	v_add_f32_e32 v179, v99, v179
	s_waitcnt lgkmcnt(6)
	v_mfma_f32_32x32x16_bf16 v[52:67], v[166:169], v[104:107], v[52:67]
	ds_read_b128 v[166:169], v205 offset:45056
	v_exp_f32_e32 v77, v77
	v_add_f32_e32 v179, v76, v179
	v_cvt_pk_bf16_f32 v123, v98, v99
	v_exp_f32_e32 v78, v78
	s_waitcnt lgkmcnt(5)
	v_mfma_f32_32x32x16_bf16 v[36:51], v[170:173], v[108:111], v[36:51]
	ds_read_b128 v[170:173], v205 offset:51712
	v_add_f32_e32 v179, v77, v179
	v_exp_f32_e32 v79, v79
	v_add_f32_e32 v179, v78, v179
	v_cvt_pk_bf16_f32 v128, v76, v77
	s_waitcnt lgkmcnt(4)
	v_mfma_f32_32x32x16_bf16 v[52:67], v[174:177], v[108:111], v[52:67]
	ds_read_b128 v[174:177], v205 offset:45088
	v_exp_f32_e32 v80, v80
	v_add_f32_e32 v179, v79, v179
	v_exp_f32_e32 v81, v81
	v_add_f32_e32 v179, v80, v179
	s_waitcnt lgkmcnt(4)
	v_mfma_f32_32x32x16_bf16 v[36:51], v[206:209], v[112:115], v[36:51]
	ds_read_b128 v[206:209], v205 offset:51744
	v_cvt_pk_bf16_f32 v129, v78, v79
	v_exp_f32_e32 v82, v82
	v_add_f32_e32 v179, v81, v179
	v_exp_f32_e32 v83, v83
	s_waitcnt lgkmcnt(4)
	v_mfma_f32_32x32x16_bf16 v[52:67], v[226:229], v[112:115], v[52:67]
	ds_read_b128 v[226:229], v205 offset:45120
	v_add_f32_e32 v179, v82, v179
	v_cvt_pk_bf16_f32 v130, v80, v81
	v_add_f32_e32 v179, v83, v179
	v_cvt_pk_bf16_f32 v131, v82, v83
	v_add_f32_e32 v224, v224, v179
	s_add_i32 s1, s1, 1
	s_cmp_lt_u32 s1, s34
	s_barrier
	s_cbranch_scc0 .Latt_u10_fin0
	s_waitcnt lgkmcnt(4)
	v_mfma_f32_32x32x16_bf16 v[84:99], v[166:169], v[132:135], 0
	ds_read_b128 v[166:169], v205 offset:51776
	v_exp_f32_e32 v20, v20
	v_exp_f32_e32 v4, v4
	v_exp_f32_e32 v21, v21
	s_waitcnt lgkmcnt(4)
	v_mfma_f32_32x32x16_bf16 v[68:83], v[170:173], v[132:135], 0
	ds_read_b128 v[170:173], v205 offset:45152
	v_add_f32_e32 v179, v4, v20
	v_exp_f32_e32 v5, v5
	v_add_f32_e32 v179, v21, v179
	v_cvt_pk_bf16_f32 v100, v20, v21
	s_waitcnt lgkmcnt(4)
	v_mfma_f32_32x32x16_bf16 v[84:99], v[174:177], v[136:139], v[84:99]
	ds_read_b128 v[174:177], v205 offset:51808
	v_exp_f32_e32 v22, v22
	v_add_f32_e32 v179, v5, v179
	v_exp_f32_e32 v6, v6
	v_add_f32_e32 v179, v22, v179
	s_waitcnt lgkmcnt(4)
	v_mfma_f32_32x32x16_bf16 v[68:83], v[206:209], v[136:139], v[68:83]
	ds_read_b128 v[206:209], v205 offset:45184
	v_cvt_pk_bf16_f32 v108, v4, v5
	v_exp_f32_e32 v23, v23
	v_add_f32_e32 v179, v6, v179
	v_exp_f32_e32 v7, v7
	s_waitcnt lgkmcnt(4)
	v_mfma_f32_32x32x16_bf16 v[84:99], v[226:229], v[140:143], v[84:99]
	ds_read_b128 v[226:229], v205 offset:51840
	v_add_f32_e32 v179, v23, v179
	v_cvt_pk_bf16_f32 v101, v22, v23
	v_exp_f32_e32 v24, v24
	v_add_f32_e32 v179, v7, v179
	s_waitcnt lgkmcnt(4)
	v_mfma_f32_32x32x16_bf16 v[68:83], v[166:169], v[140:143], v[68:83]
	ds_read_b128 v[166:169], v205 offset:45216
	v_exp_f32_e32 v8, v8
	v_add_f32_e32 v179, v24, v179
	v_cvt_pk_bf16_f32 v109, v6, v7
	v_exp_f32_e32 v25, v25
	s_waitcnt lgkmcnt(4)
	v_mfma_f32_32x32x16_bf16 v[84:99], v[170:173], v[144:147], v[84:99]
	ds_read_b128 v[170:173], v205 offset:51872
	v_add_f32_e32 v179, v8, v179
	v_exp_f32_e32 v9, v9
	v_add_f32_e32 v179, v25, v179
	v_cvt_pk_bf16_f32 v102, v24, v25
	s_waitcnt lgkmcnt(4)
	v_mfma_f32_32x32x16_bf16 v[68:83], v[174:177], v[144:147], v[68:83]
	ds_read_b128 v[174:177], v178 offset:26624
	v_exp_f32_e32 v26, v26
	v_add_f32_e32 v179, v9, v179
	v_exp_f32_e32 v10, v10
	v_add_f32_e32 v179, v26, v179
	s_waitcnt lgkmcnt(4)
	v_mfma_f32_32x32x16_bf16 v[84:99], v[206:209], v[148:151], v[84:99]
	ds_read_b128 v[206:209], v178 offset:31232
	s_waitcnt vmcnt(0)
	ds_write_b128 v219, v[156:159] offset:0
	v_cvt_pk_bf16_f32 v110, v8, v9
	v_exp_f32_e32 v27, v27
	v_add_f32_e32 v179, v10, v179
	v_exp_f32_e32 v11, v11
	s_waitcnt lgkmcnt(5)
	v_mfma_f32_32x32x16_bf16 v[68:83], v[226:229], v[148:151], v[68:83]
	ds_read_b128 v[226:229], v178 offset:26656
	ds_write_b64 v220, v[160:161] offset:0
	v_add_f32_e32 v179, v27, v179
	v_cvt_pk_bf16_f32 v103, v26, v27
	v_exp_f32_e32 v28, v28
	v_add_f32_e32 v179, v11, v179
	s_waitcnt lgkmcnt(6)
	v_mfma_f32_32x32x16_bf16 v[84:99], v[166:169], v[152:155], v[84:99]
	ds_read_b128 v[166:169], v178 offset:31264
	ds_write_b64 v234, v[162:163] offset:28672
	v_exp_f32_e32 v29, v29
	v_add_f32_e32 v179, v28, v179
	v_cvt_pk_bf16_f32 v111, v10, v11
	v_exp_f32_e32 v30, v30
	s_waitcnt lgkmcnt(7)
	v_mfma_f32_32x32x16_bf16 v[68:83], v[170:173], v[152:155], v[68:83]
	ds_read_b128 v[170:173], v178 offset:26688
	ds_write_b64 v235, v[164:165] offset:28672
	v_add_f32_e32 v179, v29, v179
	v_exp_f32_e32 v31, v31
	v_add_f32_e32 v179, v30, v179
	v_cvt_pk_bf16_f32 v104, v28, v29
	s_waitcnt lgkmcnt(8)
	v_mfma_f32_32x32x16_bf16 v[36:51], v[174:177], v[116:119], v[36:51]
	ds_read_b128 v[174:177], v178 offset:31296
	v_lshl_add_u32 v156, s12, v215, v223
	global_load_dwordx4 v[156:159], v156, s[44:45]
	v_exp_f32_e32 v32, v32
	v_add_f32_e32 v179, v31, v179
	v_exp_f32_e32 v33, v33
	v_add_f32_e32 v179, v32, v179
	s_waitcnt lgkmcnt(8)
	v_mfma_f32_32x32x16_bf16 v[52:67], v[206:209], v[116:119], v[52:67]
	ds_read_b128 v[206:209], v178 offset:26720
	v_mad_u32_u24 v160, s12, v199, v202
	global_load_dwordx2 v[160:161], v160, s[44:45]
	s_add_i32 s12, s12, 1
	s_cmp_eq_u32 s12, s34
	s_cselect_b32 s12, 0, s12
	v_cvt_pk_bf16_f32 v105, v30, v31
	v_exp_f32_e32 v34, v34
	v_add_f32_e32 v179, v33, v179
	v_exp_f32_e32 v35, v35
	s_waitcnt lgkmcnt(7)
	v_mfma_f32_32x32x16_bf16 v[36:51], v[226:229], v[120:123], v[36:51]
	ds_read_b128 v[226:229], v178 offset:31328
	v_lshl_add_u32 v162, s13, 7, v204
	global_load_dwordx4 v[162:165], v162, s[44:45]
	s_add_i32 s13, s13, 1
	s_cmp_eq_u32 s13, s34
	s_cselect_b32 s13, 0, s13
	v_add_f32_e32 v179, v34, v179
	v_cvt_pk_bf16_f32 v106, v32, v33
	v_exp_f32_e32 v12, v12
	v_add_f32_e32 v179, v35, v179
	s_waitcnt lgkmcnt(6)
	v_mfma_f32_32x32x16_bf16 v[52:67], v[166:169], v[120:123], v[52:67]
	ds_read_b128 v[166:169], v205 offset:58368
	v_exp_f32_e32 v13, v13
	v_add_f32_e32 v179, v12, v179
	v_cvt_pk_bf16_f32 v107, v34, v35
	v_exp_f32_e32 v14, v14
	s_waitcnt lgkmcnt(5)
	v_mfma_f32_32x32x16_bf16 v[36:51], v[170:173], v[124:127], v[36:51]
	ds_read_b128 v[170:173], v205 offset:65024
	v_add_f32_e32 v179, v13, v179
	v_exp_f32_e32 v15, v15
	v_add_f32_e32 v179, v14, v179
	v_cvt_pk_bf16_f32 v112, v12, v13
	s_waitcnt lgkmcnt(4)
	v_mfma_f32_32x32x16_bf16 v[52:67], v[174:177], v[124:127], v[52:67]
	ds_read_b128 v[174:177], v205 offset:58400
	v_exp_f32_e32 v16, v16
	v_add_f32_e32 v179, v15, v179
	v_exp_f32_e32 v17, v17
	v_add_f32_e32 v179, v16, v179
	s_waitcnt lgkmcnt(4)
	v_mfma_f32_32x32x16_bf16 v[36:51], v[206:209], v[128:131], v[36:51]
	ds_read_b128 v[206:209], v205 offset:65056
	v_cvt_pk_bf16_f32 v113, v14, v15
	v_exp_f32_e32 v18, v18
	v_add_f32_e32 v179, v17, v179
	v_exp_f32_e32 v19, v19
	s_waitcnt lgkmcnt(4)
	v_mfma_f32_32x32x16_bf16 v[52:67], v[226:229], v[128:131], v[52:67]
	ds_read_b128 v[226:229], v205 offset:58432
	v_add_f32_e32 v179, v18, v179
	v_cvt_pk_bf16_f32 v114, v16, v17
	v_add_f32_e32 v179, v19, v179
	v_cvt_pk_bf16_f32 v115, v18, v19
	v_add_f32_e32 v224, v224, v179
	s_add_i32 s1, s1, 1
	s_waitcnt lgkmcnt(4)
	v_mfma_f32_32x32x16_bf16 v[20:35], v[166:169], v[132:135], 0
	ds_read_b128 v[166:169], v205 offset:65088
	v_exp_f32_e32 v84, v84
	v_exp_f32_e32 v68, v68
	v_exp_f32_e32 v85, v85
	s_waitcnt lgkmcnt(4)
	v_mfma_f32_32x32x16_bf16 v[4:19], v[170:173], v[132:135], 0
	ds_read_b128 v[170:173], v205 offset:58464
	v_add_f32_e32 v179, v68, v84
	v_exp_f32_e32 v69, v69
	v_add_f32_e32 v179, v85, v179
	v_cvt_pk_bf16_f32 v116, v84, v85
	s_waitcnt lgkmcnt(4)
	v_mfma_f32_32x32x16_bf16 v[20:35], v[174:177], v[136:139], v[20:35]
	ds_read_b128 v[174:177], v205 offset:65120
	v_exp_f32_e32 v86, v86
	v_add_f32_e32 v179, v69, v179
	v_exp_f32_e32 v70, v70
	v_add_f32_e32 v179, v86, v179
	s_waitcnt lgkmcnt(4)
	v_mfma_f32_32x32x16_bf16 v[4:19], v[206:209], v[136:139], v[4:19]
	ds_read_b128 v[206:209], v205 offset:58496
	v_cvt_pk_bf16_f32 v124, v68, v69
	v_exp_f32_e32 v87, v87
	v_add_f32_e32 v179, v70, v179
	v_exp_f32_e32 v71, v71
	s_waitcnt lgkmcnt(4)
	v_mfma_f32_32x32x16_bf16 v[20:35], v[226:229], v[140:143], v[20:35]
	ds_read_b128 v[226:229], v205 offset:65152
	v_add_f32_e32 v179, v87, v179
	v_cvt_pk_bf16_f32 v117, v86, v87
	v_exp_f32_e32 v88, v88
	v_add_f32_e32 v179, v71, v179
	s_waitcnt lgkmcnt(4)
	v_mfma_f32_32x32x16_bf16 v[4:19], v[166:169], v[140:143], v[4:19]
	ds_read_b128 v[166:169], v205 offset:58528
	v_exp_f32_e32 v72, v72
	v_add_f32_e32 v179, v88, v179
	v_cvt_pk_bf16_f32 v125, v70, v71
	v_exp_f32_e32 v89, v89
	s_waitcnt lgkmcnt(4)
	v_mfma_f32_32x32x16_bf16 v[20:35], v[170:173], v[144:147], v[20:35]
	ds_read_b128 v[170:173], v205 offset:65184
	v_add_f32_e32 v179, v72, v179
	v_exp_f32_e32 v73, v73
	v_add_f32_e32 v179, v89, v179
	v_cvt_pk_bf16_f32 v118, v88, v89
	s_waitcnt lgkmcnt(4)
	v_mfma_f32_32x32x16_bf16 v[4:19], v[174:177], v[144:147], v[4:19]
	ds_read_b128 v[174:177], v178 offset:35840
	v_exp_f32_e32 v90, v90
	v_add_f32_e32 v179, v73, v179
	v_exp_f32_e32 v74, v74
	v_add_f32_e32 v179, v90, v179
	s_waitcnt lgkmcnt(4)
	v_mfma_f32_32x32x16_bf16 v[20:35], v[206:209], v[148:151], v[20:35]
	ds_read_b128 v[206:209], v178 offset:40448
	s_waitcnt vmcnt(0)
	ds_write_b128 v219, v[156:159] offset:13312
	v_cvt_pk_bf16_f32 v126, v72, v73
	v_exp_f32_e32 v91, v91
	v_add_f32_e32 v179, v74, v179
	v_exp_f32_e32 v75, v75
	s_waitcnt lgkmcnt(5)
	v_mfma_f32_32x32x16_bf16 v[4:19], v[226:229], v[148:151], v[4:19]
	ds_read_b128 v[226:229], v178 offset:35872
	ds_write_b64 v220, v[160:161] offset:13312
	v_add_f32_e32 v179, v91, v179
	v_cvt_pk_bf16_f32 v119, v90, v91
	v_exp_f32_e32 v92, v92
	v_add_f32_e32 v179, v75, v179
	s_waitcnt lgkmcnt(6)
	v_mfma_f32_32x32x16_bf16 v[20:35], v[166:169], v[152:155], v[20:35]
	ds_read_b128 v[166:169], v178 offset:40480
	ds_write_b64 v234, v[162:163] offset:37888
	v_exp_f32_e32 v93, v93
	v_add_f32_e32 v179, v92, v179
	v_cvt_pk_bf16_f32 v127, v74, v75
	v_exp_f32_e32 v94, v94
	s_waitcnt lgkmcnt(7)
	v_mfma_f32_32x32x16_bf16 v[4:19], v[170:173], v[152:155], v[4:19]
	ds_read_b128 v[170:173], v178 offset:35904
	ds_write_b64 v235, v[164:165] offset:37888
	v_add_f32_e32 v179, v93, v179
	v_exp_f32_e32 v95, v95
	v_add_f32_e32 v179, v94, v179
	v_cvt_pk_bf16_f32 v120, v92, v93
	s_waitcnt lgkmcnt(8)
	v_mfma_f32_32x32x16_bf16 v[36:51], v[174:177], v[100:103], v[36:51]
	ds_read_b128 v[174:177], v178 offset:40512
	v_lshl_add_u32 v156, s12, v215, v223
	global_load_dwordx4 v[156:159], v156, s[44:45]
	v_exp_f32_e32 v96, v96
	v_add_f32_e32 v179, v95, v179
	v_exp_f32_e32 v97, v97
	v_add_f32_e32 v179, v96, v179
	s_waitcnt lgkmcnt(8)
	v_mfma_f32_32x32x16_bf16 v[52:67], v[206:209], v[100:103], v[52:67]
	ds_read_b128 v[206:209], v178 offset:35936
	v_mad_u32_u24 v160, s12, v199, v202
	global_load_dwordx2 v[160:161], v160, s[44:45]
	s_add_i32 s12, s12, 1
	s_cmp_eq_u32 s12, s34
	s_cselect_b32 s12, 0, s12
	v_cvt_pk_bf16_f32 v121, v94, v95
	v_exp_f32_e32 v98, v98
	v_add_f32_e32 v179, v97, v179
	v_exp_f32_e32 v99, v99
	s_waitcnt lgkmcnt(7)
	v_mfma_f32_32x32x16_bf16 v[36:51], v[226:229], v[104:107], v[36:51]
	ds_read_b128 v[226:229], v178 offset:40544
	v_lshl_add_u32 v162, s13, 7, v204
	global_load_dwordx4 v[162:165], v162, s[44:45]
	s_add_i32 s13, s13, 1
	s_cmp_eq_u32 s13, s34
	s_cselect_b32 s13, 0, s13
	v_add_f32_e32 v179, v98, v179
	v_cvt_pk_bf16_f32 v122, v96, v97
	v_exp_f32_e32 v76, v76
	v_add_f32_e32 v179, v99, v179
	s_waitcnt lgkmcnt(6)
	v_mfma_f32_32x32x16_bf16 v[52:67], v[166:169], v[104:107], v[52:67]
	ds_read_b128 v[166:169], v230 offset:6144
	v_exp_f32_e32 v77, v77
	v_add_f32_e32 v179, v76, v179
	v_cvt_pk_bf16_f32 v123, v98, v99
	v_exp_f32_e32 v78, v78
	s_waitcnt lgkmcnt(5)
	v_mfma_f32_32x32x16_bf16 v[36:51], v[170:173], v[108:111], v[36:51]
	ds_read_b128 v[170:173], v230 offset:12800
	v_add_f32_e32 v179, v77, v179
	v_exp_f32_e32 v79, v79
	v_add_f32_e32 v179, v78, v179
	v_cvt_pk_bf16_f32 v128, v76, v77
	s_waitcnt lgkmcnt(4)
	v_mfma_f32_32x32x16_bf16 v[52:67], v[174:177], v[108:111], v[52:67]
	ds_read_b128 v[174:177], v230 offset:6176
	v_exp_f32_e32 v80, v80
	v_add_f32_e32 v179, v79, v179
	v_exp_f32_e32 v81, v81
	v_add_f32_e32 v179, v80, v179
	s_waitcnt lgkmcnt(4)
	v_mfma_f32_32x32x16_bf16 v[36:51], v[206:209], v[112:115], v[36:51]
	ds_read_b128 v[206:209], v230 offset:12832
	v_cvt_pk_bf16_f32 v129, v78, v79
	v_exp_f32_e32 v82, v82
	v_add_f32_e32 v179, v81, v179
	v_exp_f32_e32 v83, v83
	s_waitcnt lgkmcnt(4)
	v_mfma_f32_32x32x16_bf16 v[52:67], v[226:229], v[112:115], v[52:67]
	ds_read_b128 v[226:229], v230 offset:6208
	v_add_f32_e32 v179, v82, v179
	v_cvt_pk_bf16_f32 v130, v80, v81
	v_add_f32_e32 v179, v83, v179
	v_cvt_pk_bf16_f32 v131, v82, v83
	v_add_f32_e32 v224, v224, v179
	s_add_i32 s1, s1, 1
	s_cmp_lt_u32 s1, s34
	s_barrier
	s_cbranch_scc0 .Latt_u10_fin2
	s_waitcnt lgkmcnt(4)
	v_mfma_f32_32x32x16_bf16 v[84:99], v[166:169], v[132:135], 0
	ds_read_b128 v[166:169], v230 offset:12864
	v_exp_f32_e32 v20, v20
	v_exp_f32_e32 v4, v4
	v_exp_f32_e32 v21, v21
	s_waitcnt lgkmcnt(4)
	v_mfma_f32_32x32x16_bf16 v[68:83], v[170:173], v[132:135], 0
	ds_read_b128 v[170:173], v230 offset:6240
	v_add_f32_e32 v179, v4, v20
	v_exp_f32_e32 v5, v5
	v_add_f32_e32 v179, v21, v179
	v_cvt_pk_bf16_f32 v100, v20, v21
	s_waitcnt lgkmcnt(4)
	v_mfma_f32_32x32x16_bf16 v[84:99], v[174:177], v[136:139], v[84:99]
	ds_read_b128 v[174:177], v230 offset:12896
	v_exp_f32_e32 v22, v22
	v_add_f32_e32 v179, v5, v179
	v_exp_f32_e32 v6, v6
	v_add_f32_e32 v179, v22, v179
	s_waitcnt lgkmcnt(4)
	v_mfma_f32_32x32x16_bf16 v[68:83], v[206:209], v[136:139], v[68:83]
	ds_read_b128 v[206:209], v230 offset:6272
	v_cvt_pk_bf16_f32 v108, v4, v5
	v_exp_f32_e32 v23, v23
	v_add_f32_e32 v179, v6, v179
	v_exp_f32_e32 v7, v7
	s_waitcnt lgkmcnt(4)
	v_mfma_f32_32x32x16_bf16 v[84:99], v[226:229], v[140:143], v[84:99]
	ds_read_b128 v[226:229], v230 offset:12928
	v_add_f32_e32 v179, v23, v179
	v_cvt_pk_bf16_f32 v101, v22, v23
	v_exp_f32_e32 v24, v24
	v_add_f32_e32 v179, v7, v179
	s_waitcnt lgkmcnt(4)
	v_mfma_f32_32x32x16_bf16 v[68:83], v[166:169], v[140:143], v[68:83]
	ds_read_b128 v[166:169], v230 offset:6304
	v_exp_f32_e32 v8, v8
	v_add_f32_e32 v179, v24, v179
	v_cvt_pk_bf16_f32 v109, v6, v7
	v_exp_f32_e32 v25, v25
	s_waitcnt lgkmcnt(4)
	v_mfma_f32_32x32x16_bf16 v[84:99], v[170:173], v[144:147], v[84:99]
	ds_read_b128 v[170:173], v230 offset:12960
	v_add_f32_e32 v179, v8, v179
	v_exp_f32_e32 v9, v9
	v_add_f32_e32 v179, v25, v179
	v_cvt_pk_bf16_f32 v102, v24, v25
	s_waitcnt lgkmcnt(4)
	v_mfma_f32_32x32x16_bf16 v[68:83], v[174:177], v[144:147], v[68:83]
	ds_read_b128 v[174:177], v231 offset:19456
	v_exp_f32_e32 v26, v26
	v_add_f32_e32 v179, v9, v179
	v_exp_f32_e32 v10, v10
	v_add_f32_e32 v179, v26, v179
	s_waitcnt lgkmcnt(4)
	v_mfma_f32_32x32x16_bf16 v[84:99], v[206:209], v[148:151], v[84:99]
	ds_read_b128 v[206:209], v231 offset:24064
	s_waitcnt vmcnt(0)
	ds_write_b128 v219, v[156:159] offset:45056
	v_cvt_pk_bf16_f32 v110, v8, v9
	v_exp_f32_e32 v27, v27
	v_add_f32_e32 v179, v10, v179
	v_exp_f32_e32 v11, v11
	s_waitcnt lgkmcnt(5)
	v_mfma_f32_32x32x16_bf16 v[68:83], v[226:229], v[148:151], v[68:83]
	ds_read_b128 v[226:229], v231 offset:19488
	ds_write_b64 v220, v[160:161] offset:45056
	v_add_f32_e32 v179, v27, v179
	v_cvt_pk_bf16_f32 v103, v26, v27
	v_exp_f32_e32 v28, v28
	v_add_f32_e32 v179, v11, v179
	s_waitcnt lgkmcnt(6)
	v_mfma_f32_32x32x16_bf16 v[84:99], v[166:169], v[152:155], v[84:99]
	ds_read_b128 v[166:169], v231 offset:24096
	ds_write_b64 v221, v[162:163] offset:26624
	v_exp_f32_e32 v29, v29
	v_add_f32_e32 v179, v28, v179
	v_cvt_pk_bf16_f32 v111, v10, v11
	v_exp_f32_e32 v30, v30
	s_waitcnt lgkmcnt(7)
	v_mfma_f32_32x32x16_bf16 v[68:83], v[170:173], v[152:155], v[68:83]
	ds_read_b128 v[170:173], v231 offset:19520
	ds_write_b64 v222, v[164:165] offset:26624
	v_add_f32_e32 v179, v29, v179
	v_exp_f32_e32 v31, v31
	v_add_f32_e32 v179, v30, v179
	v_cvt_pk_bf16_f32 v104, v28, v29
	s_waitcnt lgkmcnt(8)
	v_mfma_f32_32x32x16_bf16 v[36:51], v[174:177], v[116:119], v[36:51]
	ds_read_b128 v[174:177], v231 offset:24128
	v_lshl_add_u32 v156, s12, v215, v223
	global_load_dwordx4 v[156:159], v156, s[44:45]
	v_exp_f32_e32 v32, v32
	v_add_f32_e32 v179, v31, v179
	v_exp_f32_e32 v33, v33
	v_add_f32_e32 v179, v32, v179
	s_waitcnt lgkmcnt(8)
	v_mfma_f32_32x32x16_bf16 v[52:67], v[206:209], v[116:119], v[52:67]
	ds_read_b128 v[206:209], v231 offset:19552
	v_mad_u32_u24 v160, s12, v199, v202
	global_load_dwordx2 v[160:161], v160, s[44:45]
	s_add_i32 s12, s12, 1
	s_cmp_eq_u32 s12, s34
	s_cselect_b32 s12, 0, s12
	v_cvt_pk_bf16_f32 v105, v30, v31
	v_exp_f32_e32 v34, v34
	v_add_f32_e32 v179, v33, v179
	v_exp_f32_e32 v35, v35
	s_waitcnt lgkmcnt(7)
	v_mfma_f32_32x32x16_bf16 v[36:51], v[226:229], v[120:123], v[36:51]
	ds_read_b128 v[226:229], v231 offset:24160
	v_lshl_add_u32 v162, s13, 7, v204
	global_load_dwordx4 v[162:165], v162, s[44:45]
	s_add_i32 s13, s13, 1
	s_cmp_eq_u32 s13, s34
	s_cselect_b32 s13, 0, s13
	v_add_f32_e32 v179, v34, v179
	v_cvt_pk_bf16_f32 v106, v32, v33
	v_exp_f32_e32 v12, v12
	v_add_f32_e32 v179, v35, v179
	s_waitcnt lgkmcnt(6)
	v_mfma_f32_32x32x16_bf16 v[52:67], v[166:169], v[120:123], v[52:67]
	ds_read_b128 v[166:169], v205
	v_exp_f32_e32 v13, v13
	v_add_f32_e32 v179, v12, v179
	v_cvt_pk_bf16_f32 v107, v34, v35
	v_exp_f32_e32 v14, v14
	s_waitcnt lgkmcnt(5)
	v_mfma_f32_32x32x16_bf16 v[36:51], v[170:173], v[124:127], v[36:51]
	ds_read_b128 v[170:173], v205 offset:6656
	v_add_f32_e32 v179, v13, v179
	v_exp_f32_e32 v15, v15
	v_add_f32_e32 v179, v14, v179
	v_cvt_pk_bf16_f32 v112, v12, v13
	s_waitcnt lgkmcnt(4)
	v_mfma_f32_32x32x16_bf16 v[52:67], v[174:177], v[124:127], v[52:67]
	ds_read_b128 v[174:177], v205 offset:32
	v_exp_f32_e32 v16, v16
	v_add_f32_e32 v179, v15, v179
	v_exp_f32_e32 v17, v17
	v_add_f32_e32 v179, v16, v179
	s_waitcnt lgkmcnt(4)
	v_mfma_f32_32x32x16_bf16 v[36:51], v[206:209], v[128:131], v[36:51]
	ds_read_b128 v[206:209], v205 offset:6688
	v_cvt_pk_bf16_f32 v113, v14, v15
	v_exp_f32_e32 v18, v18
	v_add_f32_e32 v179, v17, v179
	v_exp_f32_e32 v19, v19
	s_waitcnt lgkmcnt(4)
	v_mfma_f32_32x32x16_bf16 v[52:67], v[226:229], v[128:131], v[52:67]
	ds_read_b128 v[226:229], v205 offset:64
	v_add_f32_e32 v179, v18, v179
	v_cvt_pk_bf16_f32 v114, v16, v17
	v_add_f32_e32 v179, v19, v179
	v_cvt_pk_bf16_f32 v115, v18, v19
	v_add_f32_e32 v224, v224, v179
	s_add_i32 s1, s1, 1
	s_waitcnt lgkmcnt(4)
	v_mfma_f32_32x32x16_bf16 v[20:35], v[166:169], v[132:135], 0
	ds_read_b128 v[166:169], v205 offset:6720
	v_exp_f32_e32 v84, v84
	v_exp_f32_e32 v68, v68
	v_exp_f32_e32 v85, v85
	s_waitcnt lgkmcnt(4)
	v_mfma_f32_32x32x16_bf16 v[4:19], v[170:173], v[132:135], 0
	ds_read_b128 v[170:173], v205 offset:96
	v_add_f32_e32 v179, v68, v84
	v_exp_f32_e32 v69, v69
	v_add_f32_e32 v179, v85, v179
	v_cvt_pk_bf16_f32 v116, v84, v85
	s_waitcnt lgkmcnt(4)
	v_mfma_f32_32x32x16_bf16 v[20:35], v[174:177], v[136:139], v[20:35]
	ds_read_b128 v[174:177], v205 offset:6752
	v_exp_f32_e32 v86, v86
	v_add_f32_e32 v179, v69, v179
	v_exp_f32_e32 v70, v70
	v_add_f32_e32 v179, v86, v179
	s_waitcnt lgkmcnt(4)
	v_mfma_f32_32x32x16_bf16 v[4:19], v[206:209], v[136:139], v[4:19]
	ds_read_b128 v[206:209], v205 offset:128
	v_cvt_pk_bf16_f32 v124, v68, v69
	v_exp_f32_e32 v87, v87
	v_add_f32_e32 v179, v70, v179
	v_exp_f32_e32 v71, v71
	s_waitcnt lgkmcnt(4)
	v_mfma_f32_32x32x16_bf16 v[20:35], v[226:229], v[140:143], v[20:35]
	ds_read_b128 v[226:229], v205 offset:6784
	v_add_f32_e32 v179, v87, v179
	v_cvt_pk_bf16_f32 v117, v86, v87
	v_exp_f32_e32 v88, v88
	v_add_f32_e32 v179, v71, v179
	s_waitcnt lgkmcnt(4)
	v_mfma_f32_32x32x16_bf16 v[4:19], v[166:169], v[140:143], v[4:19]
	ds_read_b128 v[166:169], v205 offset:160
	v_exp_f32_e32 v72, v72
	v_add_f32_e32 v179, v88, v179
	v_cvt_pk_bf16_f32 v125, v70, v71
	v_exp_f32_e32 v89, v89
	s_waitcnt lgkmcnt(4)
	v_mfma_f32_32x32x16_bf16 v[20:35], v[170:173], v[144:147], v[20:35]
	ds_read_b128 v[170:173], v205 offset:6816
	v_add_f32_e32 v179, v72, v179
	v_exp_f32_e32 v73, v73
	v_add_f32_e32 v179, v89, v179
	v_cvt_pk_bf16_f32 v118, v88, v89
	s_waitcnt lgkmcnt(4)
	v_mfma_f32_32x32x16_bf16 v[4:19], v[174:177], v[144:147], v[4:19]
	ds_read_b128 v[174:177], v231 offset:28672
	v_exp_f32_e32 v90, v90
	v_add_f32_e32 v179, v73, v179
	v_exp_f32_e32 v74, v74
	v_add_f32_e32 v179, v90, v179
	s_waitcnt lgkmcnt(4)
	v_mfma_f32_32x32x16_bf16 v[20:35], v[206:209], v[148:151], v[20:35]
	ds_read_b128 v[206:209], v231 offset:33280
	s_waitcnt vmcnt(0)
	ds_write_b128 v219, v[156:159] offset:58368
	v_cvt_pk_bf16_f32 v126, v72, v73
	v_exp_f32_e32 v91, v91
	v_add_f32_e32 v179, v74, v179
	v_exp_f32_e32 v75, v75
	s_waitcnt lgkmcnt(5)
	v_mfma_f32_32x32x16_bf16 v[4:19], v[226:229], v[148:151], v[4:19]
	ds_read_b128 v[226:229], v231 offset:28704
	ds_write_b64 v220, v[160:161] offset:58368
	v_add_f32_e32 v179, v91, v179
	v_cvt_pk_bf16_f32 v119, v90, v91
	v_exp_f32_e32 v92, v92
	v_add_f32_e32 v179, v75, v179
	s_waitcnt lgkmcnt(6)
	v_mfma_f32_32x32x16_bf16 v[20:35], v[166:169], v[152:155], v[20:35]
	ds_read_b128 v[166:169], v231 offset:33312
	ds_write_b64 v221, v[162:163] offset:35840
	v_exp_f32_e32 v93, v93
	v_add_f32_e32 v179, v92, v179
	v_cvt_pk_bf16_f32 v127, v74, v75
	v_exp_f32_e32 v94, v94
	s_waitcnt lgkmcnt(7)
	v_mfma_f32_32x32x16_bf16 v[4:19], v[170:173], v[152:155], v[4:19]
	ds_read_b128 v[170:173], v231 offset:28736
	ds_write_b64 v222, v[164:165] offset:35840
	v_add_f32_e32 v179, v93, v179
	v_exp_f32_e32 v95, v95
	v_add_f32_e32 v179, v94, v179
	v_cvt_pk_bf16_f32 v120, v92, v93
	s_waitcnt lgkmcnt(8)
	v_mfma_f32_32x32x16_bf16 v[36:51], v[174:177], v[100:103], v[36:51]
	ds_read_b128 v[174:177], v231 offset:33344
	v_lshl_add_u32 v156, s12, v215, v223
	global_load_dwordx4 v[156:159], v156, s[44:45]
	v_exp_f32_e32 v96, v96
	v_add_f32_e32 v179, v95, v179
	v_exp_f32_e32 v97, v97
	v_add_f32_e32 v179, v96, v179
	s_waitcnt lgkmcnt(8)
	v_mfma_f32_32x32x16_bf16 v[52:67], v[206:209], v[100:103], v[52:67]
	ds_read_b128 v[206:209], v231 offset:28768
	v_mad_u32_u24 v160, s12, v199, v202
	global_load_dwordx2 v[160:161], v160, s[44:45]
	s_add_i32 s12, s12, 1
	s_cmp_eq_u32 s12, s34
	s_cselect_b32 s12, 0, s12
	v_cvt_pk_bf16_f32 v121, v94, v95
	v_exp_f32_e32 v98, v98
	v_add_f32_e32 v179, v97, v179
	v_exp_f32_e32 v99, v99
	s_waitcnt lgkmcnt(7)
	v_mfma_f32_32x32x16_bf16 v[36:51], v[226:229], v[104:107], v[36:51]
	ds_read_b128 v[226:229], v231 offset:33376
	v_lshl_add_u32 v162, s13, 7, v204
	global_load_dwordx4 v[162:165], v162, s[44:45]
	s_add_i32 s13, s13, 1
	s_cmp_eq_u32 s13, s34
	s_cselect_b32 s13, 0, s13
	v_add_f32_e32 v179, v98, v179
	v_cvt_pk_bf16_f32 v122, v96, v97
	v_exp_f32_e32 v76, v76
	v_add_f32_e32 v179, v99, v179
	s_waitcnt lgkmcnt(6)
	v_mfma_f32_32x32x16_bf16 v[52:67], v[166:169], v[104:107], v[52:67]
	ds_read_b128 v[166:169], v205 offset:13312
	v_exp_f32_e32 v77, v77
	v_add_f32_e32 v179, v76, v179
	v_cvt_pk_bf16_f32 v123, v98, v99
	v_exp_f32_e32 v78, v78
	s_waitcnt lgkmcnt(5)
	v_mfma_f32_32x32x16_bf16 v[36:51], v[170:173], v[108:111], v[36:51]
	ds_read_b128 v[170:173], v205 offset:19968
	v_add_f32_e32 v179, v77, v179
	v_exp_f32_e32 v79, v79
	v_add_f32_e32 v179, v78, v179
	v_cvt_pk_bf16_f32 v128, v76, v77
	s_waitcnt lgkmcnt(4)
	v_mfma_f32_32x32x16_bf16 v[52:67], v[174:177], v[108:111], v[52:67]
	ds_read_b128 v[174:177], v205 offset:13344
	v_exp_f32_e32 v80, v80
	v_add_f32_e32 v179, v79, v179
	v_exp_f32_e32 v81, v81
	v_add_f32_e32 v179, v80, v179
	s_waitcnt lgkmcnt(4)
	v_mfma_f32_32x32x16_bf16 v[36:51], v[206:209], v[112:115], v[36:51]
	ds_read_b128 v[206:209], v205 offset:20000
	v_cvt_pk_bf16_f32 v129, v78, v79
	v_exp_f32_e32 v82, v82
	v_add_f32_e32 v179, v81, v179
	v_exp_f32_e32 v83, v83
	s_waitcnt lgkmcnt(4)
	v_mfma_f32_32x32x16_bf16 v[52:67], v[226:229], v[112:115], v[52:67]
	ds_read_b128 v[226:229], v205 offset:13376
	v_add_f32_e32 v179, v82, v179
	v_cvt_pk_bf16_f32 v130, v80, v81
	v_add_f32_e32 v179, v83, v179
	v_cvt_pk_bf16_f32 v131, v82, v83
	v_add_f32_e32 v224, v224, v179
	s_add_i32 s1, s1, 1
	s_cmp_lt_u32 s1, s34
	s_barrier
	s_cbranch_scc0 .Latt_u10_fin4
	s_waitcnt lgkmcnt(4)
	v_mfma_f32_32x32x16_bf16 v[84:99], v[166:169], v[132:135], 0
	ds_read_b128 v[166:169], v205 offset:20032
	v_exp_f32_e32 v20, v20
	v_exp_f32_e32 v4, v4
	v_exp_f32_e32 v21, v21
	s_waitcnt lgkmcnt(4)
	v_mfma_f32_32x32x16_bf16 v[68:83], v[170:173], v[132:135], 0
	ds_read_b128 v[170:173], v205 offset:13408
	v_add_f32_e32 v179, v4, v20
	v_exp_f32_e32 v5, v5
	v_add_f32_e32 v179, v21, v179
	v_cvt_pk_bf16_f32 v100, v20, v21
	s_waitcnt lgkmcnt(4)
	v_mfma_f32_32x32x16_bf16 v[84:99], v[174:177], v[136:139], v[84:99]
	ds_read_b128 v[174:177], v205 offset:20064
	v_exp_f32_e32 v22, v22
	v_add_f32_e32 v179, v5, v179
	v_exp_f32_e32 v6, v6
	v_add_f32_e32 v179, v22, v179
	s_waitcnt lgkmcnt(4)
	v_mfma_f32_32x32x16_bf16 v[68:83], v[206:209], v[136:139], v[68:83]
	ds_read_b128 v[206:209], v205 offset:13440
	v_cvt_pk_bf16_f32 v108, v4, v5
	v_exp_f32_e32 v23, v23
	v_add_f32_e32 v179, v6, v179
	v_exp_f32_e32 v7, v7
	s_waitcnt lgkmcnt(4)
	v_mfma_f32_32x32x16_bf16 v[84:99], v[226:229], v[140:143], v[84:99]
	ds_read_b128 v[226:229], v205 offset:20096
	v_add_f32_e32 v179, v23, v179
	v_cvt_pk_bf16_f32 v101, v22, v23
	v_exp_f32_e32 v24, v24
	v_add_f32_e32 v179, v7, v179
	s_waitcnt lgkmcnt(4)
	v_mfma_f32_32x32x16_bf16 v[68:83], v[166:169], v[140:143], v[68:83]
	ds_read_b128 v[166:169], v205 offset:13472
	v_exp_f32_e32 v8, v8
	v_add_f32_e32 v179, v24, v179
	v_cvt_pk_bf16_f32 v109, v6, v7
	v_exp_f32_e32 v25, v25
	s_waitcnt lgkmcnt(4)
	v_mfma_f32_32x32x16_bf16 v[84:99], v[170:173], v[144:147], v[84:99]
	ds_read_b128 v[170:173], v205 offset:20128
	v_add_f32_e32 v179, v8, v179
	v_exp_f32_e32 v9, v9
	v_add_f32_e32 v179, v25, v179
	v_cvt_pk_bf16_f32 v102, v24, v25
	s_waitcnt lgkmcnt(4)
	v_mfma_f32_32x32x16_bf16 v[68:83], v[174:177], v[144:147], v[68:83]
	ds_read_b128 v[174:177], v231 offset:37888
	v_exp_f32_e32 v26, v26
	v_add_f32_e32 v179, v9, v179
	v_exp_f32_e32 v10, v10
	v_add_f32_e32 v179, v26, v179
	s_waitcnt lgkmcnt(4)
	v_mfma_f32_32x32x16_bf16 v[84:99], v[206:209], v[148:151], v[84:99]
	ds_read_b128 v[206:209], v231 offset:42496
	s_waitcnt vmcnt(0)
	ds_write_b128 v232, v[156:159] offset:6144
	v_cvt_pk_bf16_f32 v110, v8, v9
	v_exp_f32_e32 v27, v27
	v_add_f32_e32 v179, v10, v179
	v_exp_f32_e32 v11, v11
	s_waitcnt lgkmcnt(5)
	v_mfma_f32_32x32x16_bf16 v[68:83], v[226:229], v[148:151], v[68:83]
	ds_read_b128 v[226:229], v231 offset:37920
	ds_write_b64 v233, v[160:161] offset:6144
	v_add_f32_e32 v179, v27, v179
	v_cvt_pk_bf16_f32 v103, v26, v27
	v_exp_f32_e32 v28, v28
	v_add_f32_e32 v179, v11, v179
	s_waitcnt lgkmcnt(6)
	v_mfma_f32_32x32x16_bf16 v[84:99], v[166:169], v[152:155], v[84:99]
	ds_read_b128 v[166:169], v231 offset:42528
	ds_write_b64 v234, v[162:163] offset:19456
	v_exp_f32_e32 v29, v29
	v_add_f32_e32 v179, v28, v179
	v_cvt_pk_bf16_f32 v111, v10, v11
	v_exp_f32_e32 v30, v30
	s_waitcnt lgkmcnt(7)
	v_mfma_f32_32x32x16_bf16 v[68:83], v[170:173], v[152:155], v[68:83]
	ds_read_b128 v[170:173], v231 offset:37952
	ds_write_b64 v235, v[164:165] offset:19456
	v_add_f32_e32 v179, v29, v179
	v_exp_f32_e32 v31, v31
	v_add_f32_e32 v179, v30, v179
	v_cvt_pk_bf16_f32 v104, v28, v29
	s_waitcnt lgkmcnt(8)
	v_mfma_f32_32x32x16_bf16 v[36:51], v[174:177], v[116:119], v[36:51]
	ds_read_b128 v[174:177], v231 offset:42560
	v_lshl_add_u32 v156, s12, v215, v223
	global_load_dwordx4 v[156:159], v156, s[44:45]
	v_exp_f32_e32 v32, v32
	v_add_f32_e32 v179, v31, v179
	v_exp_f32_e32 v33, v33
	v_add_f32_e32 v179, v32, v179
	s_waitcnt lgkmcnt(8)
	v_mfma_f32_32x32x16_bf16 v[52:67], v[206:209], v[116:119], v[52:67]
	ds_read_b128 v[206:209], v231 offset:37984
	v_mad_u32_u24 v160, s12, v199, v202
	global_load_dwordx2 v[160:161], v160, s[44:45]
	s_add_i32 s12, s12, 1
	s_cmp_eq_u32 s12, s34
	s_cselect_b32 s12, 0, s12
	v_cvt_pk_bf16_f32 v105, v30, v31
	v_exp_f32_e32 v34, v34
	v_add_f32_e32 v179, v33, v179
	v_exp_f32_e32 v35, v35
	s_waitcnt lgkmcnt(7)
	v_mfma_f32_32x32x16_bf16 v[36:51], v[226:229], v[120:123], v[36:51]
	ds_read_b128 v[226:229], v231 offset:42592
	v_lshl_add_u32 v162, s13, 7, v204
	global_load_dwordx4 v[162:165], v162, s[44:45]
	s_add_i32 s13, s13, 1
	s_cmp_eq_u32 s13, s34
	s_cselect_b32 s13, 0, s13
	v_add_f32_e32 v179, v34, v179
	v_cvt_pk_bf16_f32 v106, v32, v33
	v_exp_f32_e32 v12, v12
	v_add_f32_e32 v179, v35, v179
	s_waitcnt lgkmcnt(6)
	v_mfma_f32_32x32x16_bf16 v[52:67], v[166:169], v[120:123], v[52:67]
	ds_read_b128 v[166:169], v205 offset:45056
	v_exp_f32_e32 v13, v13
	v_add_f32_e32 v179, v12, v179
	v_cvt_pk_bf16_f32 v107, v34, v35
	v_exp_f32_e32 v14, v14
	s_waitcnt lgkmcnt(5)
	v_mfma_f32_32x32x16_bf16 v[36:51], v[170:173], v[124:127], v[36:51]
	ds_read_b128 v[170:173], v205 offset:51712
	v_add_f32_e32 v179, v13, v179
	v_exp_f32_e32 v15, v15
	v_add_f32_e32 v179, v14, v179
	v_cvt_pk_bf16_f32 v112, v12, v13
	s_waitcnt lgkmcnt(4)
	v_mfma_f32_32x32x16_bf16 v[52:67], v[174:177], v[124:127], v[52:67]
	ds_read_b128 v[174:177], v205 offset:45088
	v_exp_f32_e32 v16, v16
	v_add_f32_e32 v179, v15, v179
	v_exp_f32_e32 v17, v17
	v_add_f32_e32 v179, v16, v179
	s_waitcnt lgkmcnt(4)
	v_mfma_f32_32x32x16_bf16 v[36:51], v[206:209], v[128:131], v[36:51]
	ds_read_b128 v[206:209], v205 offset:51744
	v_cvt_pk_bf16_f32 v113, v14, v15
	v_exp_f32_e32 v18, v18
	v_add_f32_e32 v179, v17, v179
	v_exp_f32_e32 v19, v19
	s_waitcnt lgkmcnt(4)
	v_mfma_f32_32x32x16_bf16 v[52:67], v[226:229], v[128:131], v[52:67]
	ds_read_b128 v[226:229], v205 offset:45120
	v_add_f32_e32 v179, v18, v179
	v_cvt_pk_bf16_f32 v114, v16, v17
	v_add_f32_e32 v179, v19, v179
	v_cvt_pk_bf16_f32 v115, v18, v19
	v_add_f32_e32 v224, v224, v179
	s_add_i32 s1, s1, 1
	s_branch .Latt_u10_top

.Latt_u10_fin2:
	ds_read_b128 v[166:169], v231 offset:19456
	ds_read_b128 v[170:173], v231 offset:24064
	ds_read_b128 v[174:177], v231 offset:19488
	ds_read_b128 v[206:209], v231 offset:24096
	ds_read_b128 v[226:229], v231 offset:19520
	s_waitcnt lgkmcnt(4)
	v_mfma_f32_32x32x16_bf16 v[36:51], v[166:169], v[116:119], v[36:51]
	ds_read_b128 v[166:169], v231 offset:24128
	s_waitcnt lgkmcnt(4)
	v_mfma_f32_32x32x16_bf16 v[52:67], v[170:173], v[116:119], v[52:67]
	ds_read_b128 v[170:173], v231 offset:19552
	s_waitcnt lgkmcnt(4)
	v_mfma_f32_32x32x16_bf16 v[36:51], v[174:177], v[120:123], v[36:51]
	ds_read_b128 v[174:177], v231 offset:24160
	s_waitcnt lgkmcnt(4)
	v_mfma_f32_32x32x16_bf16 v[52:67], v[206:209], v[120:123], v[52:67]
	s_waitcnt lgkmcnt(3)
	v_mfma_f32_32x32x16_bf16 v[36:51], v[226:229], v[124:127], v[36:51]
	s_waitcnt lgkmcnt(2)
	v_mfma_f32_32x32x16_bf16 v[52:67], v[166:169], v[124:127], v[52:67]
	s_waitcnt lgkmcnt(1)
	v_mfma_f32_32x32x16_bf16 v[36:51], v[170:173], v[128:131], v[36:51]
	s_waitcnt lgkmcnt(0)
	v_mfma_f32_32x32x16_bf16 v[52:67], v[174:177], v[128:131], v[52:67]
	s_waitcnt vmcnt(0)
	s_branch .LBB0_1109
.Latt_u10_fin3:
	ds_read_b128 v[166:169], v231 offset:28672
	ds_read_b128 v[170:173], v231 offset:33280
	ds_read_b128 v[174:177], v231 offset:28704
	ds_read_b128 v[206:209], v231 offset:33312
	ds_read_b128 v[226:229], v231 offset:28736
	s_waitcnt lgkmcnt(4)
	v_mfma_f32_32x32x16_bf16 v[36:51], v[166:169], v[116:119], v[36:51]
	ds_read_b128 v[166:169], v231 offset:33344
	s_waitcnt lgkmcnt(4)
	v_mfma_f32_32x32x16_bf16 v[52:67], v[170:173], v[116:119], v[52:67]
	ds_read_b128 v[170:173], v231 offset:28768
	s_waitcnt lgkmcnt(4)
	v_mfma_f32_32x32x16_bf16 v[36:51], v[174:177], v[120:123], v[36:51]
	ds_read_b128 v[174:177], v231 offset:33376
	s_waitcnt lgkmcnt(4)
	v_mfma_f32_32x32x16_bf16 v[52:67], v[206:209], v[120:123], v[52:67]
	s_waitcnt lgkmcnt(3)
	v_mfma_f32_32x32x16_bf16 v[36:51], v[226:229], v[124:127], v[36:51]
	s_waitcnt lgkmcnt(2)
	v_mfma_f32_32x32x16_bf16 v[52:67], v[166:169], v[124:127], v[52:67]
	s_waitcnt lgkmcnt(1)
	v_mfma_f32_32x32x16_bf16 v[36:51], v[170:173], v[128:131], v[36:51]
	s_waitcnt lgkmcnt(0)
	v_mfma_f32_32x32x16_bf16 v[52:67], v[174:177], v[128:131], v[52:67]
	s_waitcnt vmcnt(0)
	s_branch .LBB0_1109
.Latt_u10_fin4:
	ds_read_b128 v[166:169], v231 offset:37888
	ds_read_b128 v[170:173], v231 offset:42496
	ds_read_b128 v[174:177], v231 offset:37920
	ds_read_b128 v[206:209], v231 offset:42528
	ds_read_b128 v[226:229], v231 offset:37952
	s_waitcnt lgkmcnt(4)
	v_mfma_f32_32x32x16_bf16 v[36:51], v[166:169], v[116:119], v[36:51]
	ds_read_b128 v[166:169], v231 offset:42560
	s_waitcnt lgkmcnt(4)
	v_mfma_f32_32x32x16_bf16 v[52:67], v[170:173], v[116:119], v[52:67]
	ds_read_b128 v[170:173], v231 offset:37984
	s_waitcnt lgkmcnt(4)
	v_mfma_f32_32x32x16_bf16 v[36:51], v[174:177], v[120:123], v[36:51]
	ds_read_b128 v[174:177], v231 offset:42592
	s_waitcnt lgkmcnt(4)
	v_mfma_f32_32x32x16_bf16 v[52:67], v[206:209], v[120:123], v[52:67]
	s_waitcnt lgkmcnt(3)
	v_mfma_f32_32x32x16_bf16 v[36:51], v[226:229], v[124:127], v[36:51]
	s_waitcnt lgkmcnt(2)
	v_mfma_f32_32x32x16_bf16 v[52:67], v[166:169], v[124:127], v[52:67]
	s_waitcnt lgkmcnt(1)
	v_mfma_f32_32x32x16_bf16 v[36:51], v[170:173], v[128:131], v[36:51]
	s_waitcnt lgkmcnt(0)
	v_mfma_f32_32x32x16_bf16 v[52:67], v[174:177], v[128:131], v[52:67]
	s_waitcnt vmcnt(0)
	s_branch .LBB0_1109
